# k15: staged vmcnt waits (younger-loads-only counts) in P6/P7 epilogues on top of k13
# speedup vs baseline: 1.0320x; 1.0022x over previous
;     __device__ __forceinline__ void operator()(EPI_ARGS) const {
;         const int j0 = u.pn * 128 + wc * 32 + 8 * fq, j0q = u.pn * 128 + wc * 32 + 8 * (fq & ~1);
;         f32x4 ba0, ba1, bb0, bb1; u32x4 glq[2][2], ypq[2][2][2];
;         EPI_ALD16(ba0, bglu + j0); EPI_ALD16(ba1, bglu + j0 + 4); EPI_ALD16(bb0, bglu + D + j0); EPI_ALD16(bb1, bglu + D + j0 + 4);
; #pragma unroll
;         for (int ai = 0; ai < 2; ++ai)
; #pragma unroll
;             for (int mp = 0; mp < 2; ++mp) {
;                 if (GATE_FP8) { const int rowq = u.pm * 256 + ai * 128 + wr * 64 + (2 * mp + (fq & 1)) * 16 + fr;
;                     const unsigned char* gp = (const unsigned char*)SGS + (size_t)rowq * D + j0q; EPI_ALD16(glq[ai][mp], gp); }
; #pragma unroll
;                 for (int h = 0; h < 2; ++h) { const int row = u.pm * 256 + ai * 128 + wr * 64 + (2 * mp + h) * 16 + fr; const bf16* yq = YPG + (size_t)row * D + j0; EPI_ALD16(ypq[ai][mp][h], yq); } }
;         asm volatile("s_waitcnt vmcnt(0)" : "+v"(ba0), "+v"(ba1), "+v"(bb0), "+v"(bb1), "+v"(ypq[0][0][0]), "+v"(ypq[0][0][1]), "+v"(ypq[0][1][0]), "+v"(ypq[0][1][1]), "+v"(ypq[1][0][0]), "+v"(ypq[1][0][1]), "+v"(ypq[1][1][0]), "+v"(ypq[1][1][1]));
;         if (GATE_FP8) asm volatile("" : "+v"(glq[0][0]), "+v"(glq[0][1]), "+v"(glq[1][0]), "+v"(glq[1][1]));
; #pragma unroll
;         for (int ai = 0; ai < 2; ++ai)
; #pragma unroll
;             for (int mp = 0; mp < 2; ++mp) { unsigned px[2], py[2]; unsigned gq[2][2] = {{0u, 0u}, {0u, 0u}};
;                 if (GATE_FP8) unpair16(glq[ai][mp], gq[0][0], gq[0][1], gq[1][0], gq[1][1]);
; #pragma unroll
;                 for (int h = 0; h < 2; ++h) { const int m = 2 * mp + h; const int row = u.pm * 256 + ai * 128 + wr * 64 + m * 16 + fr; const size_t off = (size_t)row * D + j0;
;                     const u32x4 yp = ypq[ai][mp][h]; float gsf[8];
;                     if (GATE_FP8) { v2u g8; g8.x = gq[h][0]; g8.y = gq[h][1]; const float k255 = 1.0f / 255.0f;
;                         gsf[0] = (float)(g8.x & 0xffu) * k255; gsf[1] = (float)((g8.x >> 8) & 0xffu) * k255; gsf[2] = (float)((g8.x >> 16) & 0xffu) * k255; gsf[3] = (float)(g8.x >> 24) * k255;
;                         gsf[4] = (float)(g8.y & 0xffu) * k255; gsf[5] = (float)((g8.y >> 8) & 0xffu) * k255; gsf[6] = (float)((g8.y >> 16) & 0xffu) * k255; gsf[7] = (float)(g8.y >> 24) * k255; }
.LBB0_906:
	s_lshl_b32 s14, s75, 7
	s_or_b32 s14, s14, s66
	v_or_b32_e32 v18, s14, v195
	v_or_b32_e32 v58, s14, v219
	s_lshl_b32 s14, s38, 8
	s_add_i32 s14, s14, s65
	v_or_b32_e32 v20, s14, v1
	v_ashrrev_i32_e32 v19, 31, v18
	v_or_b32_e32 v22, v20, v220
	v_lshlrev_b64 v[10:11], 2, v[18:19]
	v_ashrrev_i32_e32 v23, 31, v22
	v_lshl_add_u64 v[12:13], s[6:7], 0, v[10:11]
	v_lshlrev_b64 v[22:23], 11, v[22:23]
	v_lshl_add_u64 v[2:3], v[12:13], 0, 16
	v_lshl_add_u64 v[10:11], s[20:21], 0, v[10:11]
	v_ashrrev_i32_e32 v59, 31, v58
	v_lshl_add_u64 v[22:23], s[10:11], 0, v[22:23]
	s_nop 15
	s_nop 15
	global_load_dwordx4 v[6:9], v[12:13], off
	global_load_dwordx4 v[2:5], v[2:3], off
	global_load_dwordx4 v[14:17], v[10:11], off
	v_lshl_add_u64 v[10:11], v[12:13], 0, s[24:25]
	v_lshl_add_u64 v[22:23], v[22:23], 0, v[58:59]
	v_ashrrev_i32_e32 v21, 31, v20
	global_load_dwordx4 v[10:13], v[10:11], off
	global_load_dwordx4 v[62:65], v[22:23], off
	v_lshlrev_b64 v[22:23], 12, v[20:21]
	v_lshl_add_u64 v[22:23], s[12:13], 0, v[22:23]
	v_lshlrev_b64 v[18:19], 1, v[18:19]
	v_lshl_add_u64 v[22:23], v[22:23], 0, v[18:19]
	global_load_dwordx4 v[214:217], v[22:23], off
	v_or_b32_e32 v22, 16, v20
	v_ashrrev_i32_e32 v23, 31, v22
	v_lshlrev_b64 v[22:23], 12, v[22:23]
	v_lshl_add_u64 v[22:23], s[12:13], 0, v[22:23]
	v_lshl_add_u64 v[22:23], v[22:23], 0, v[18:19]
	global_load_dwordx4 v[54:57], v[22:23], off
	v_or_b32_e32 v22, v20, v221
	v_ashrrev_i32_e32 v23, 31, v22
	v_lshlrev_b64 v[22:23], 11, v[22:23]
	v_lshl_add_u64 v[22:23], s[10:11], 0, v[22:23]
	v_lshl_add_u64 v[22:23], v[22:23], 0, v[58:59]
	global_load_dwordx4 v[50:53], v[22:23], off
	v_or_b32_e32 v22, 32, v20
	v_or_b32_e32 v20, 48, v20
	v_ashrrev_i32_e32 v21, 31, v20
	v_ashrrev_i32_e32 v23, 31, v22
	v_lshlrev_b64 v[20:21], 12, v[20:21]
	v_lshlrev_b64 v[22:23], 12, v[22:23]
	v_lshl_add_u64 v[20:21], s[12:13], 0, v[20:21]
	v_lshl_add_u64 v[22:23], s[12:13], 0, v[22:23]
	v_lshl_add_u64 v[20:21], v[20:21], 0, v[18:19]
	v_lshl_add_u64 v[22:23], v[22:23], 0, v[18:19]
	global_load_dwordx4 v[46:49], v[22:23], off
	global_load_dwordx4 v[42:45], v[20:21], off
	v_add_u32_e32 v20, s14, v218
	v_or_b32_e32 v22, v20, v220
	v_ashrrev_i32_e32 v23, 31, v22
	v_lshlrev_b64 v[22:23], 11, v[22:23]
	v_lshl_add_u64 v[22:23], s[10:11], 0, v[22:23]
	v_lshl_add_u64 v[22:23], v[22:23], 0, v[58:59]
	v_ashrrev_i32_e32 v21, 31, v20
	global_load_dwordx4 v[38:41], v[22:23], off
	v_lshlrev_b64 v[22:23], 12, v[20:21]
	v_lshl_add_u64 v[22:23], s[12:13], 0, v[22:23]
	v_lshl_add_u64 v[22:23], v[22:23], 0, v[18:19]
	global_load_dwordx4 v[34:37], v[22:23], off
	v_or_b32_e32 v22, 16, v20
	v_ashrrev_i32_e32 v23, 31, v22
	v_lshlrev_b64 v[22:23], 12, v[22:23]
	v_lshl_add_u64 v[22:23], s[12:13], 0, v[22:23]
	v_lshl_add_u64 v[22:23], v[22:23], 0, v[18:19]
	global_load_dwordx4 v[30:33], v[22:23], off
	v_or_b32_e32 v22, v20, v221
	v_ashrrev_i32_e32 v23, 31, v22
	v_lshlrev_b64 v[22:23], 11, v[22:23]
	v_lshl_add_u64 v[22:23], s[10:11], 0, v[22:23]
	v_lshl_add_u64 v[22:23], v[22:23], 0, v[58:59]
	global_load_dwordx4 v[26:29], v[22:23], off
	v_or_b32_e32 v22, 32, v20
	v_or_b32_e32 v20, 48, v20
	v_ashrrev_i32_e32 v23, 31, v22
	v_ashrrev_i32_e32 v21, 31, v20
	v_lshlrev_b64 v[22:23], 12, v[22:23]
	v_lshlrev_b64 v[20:21], 12, v[20:21]
	v_lshl_add_u64 v[22:23], s[12:13], 0, v[22:23]
	v_lshl_add_u64 v[20:21], s[12:13], 0, v[20:21]
	v_lshl_add_u64 v[22:23], v[22:23], 0, v[18:19]
	v_lshl_add_u64 v[18:19], v[20:21], 0, v[18:19]
	global_load_dwordx4 v[22:25], v[22:23], off
	global_load_dwordx4 v[18:21], v[18:19], off
	v_or_b32_e32 v60, s14, v222
	s_andn2_b64 vcc, exec, s[4:5]
	s_waitcnt vmcnt(11)
	v_mov_b32_e32 v240, v65
	s_nop 1
	v_permlane16_swap_b32_e32 v63, v240
	v_cvt_f32_ubyte0_e32 v232, v63
	v_cvt_f32_ubyte1_e32 v234, v63
	v_cvt_f32_ubyte2_e32 v236, v63
	v_cvt_f32_ubyte3_e32 v238, v63
	v_fmamk_f32 v63, v182, 0x3d000000, v14
	v_mul_f32_e32 v63, 0xbfb8aa3b, v63
	v_fmamk_f32 v178, v178, 0x3d000000, v10
	v_exp_f32_e32 v63, v63
	v_mul_f32_e32 v178, 0xbfb8aa3b, v178
	v_exp_f32_e32 v178, v178
	v_fmamk_f32 v233, v186, 0x3d000000, v2
	v_add_f32_e32 v63, 1.0, v63
	v_rcp_f32_e32 v213, v63
	v_add_f32_e32 v63, 1.0, v178
	v_rcp_f32_e32 v182, v63
	v_fmamk_f32 v63, v183, 0x3d000000, v15
	v_mul_f32_e32 v63, 0xbfb8aa3b, v63
	v_fmamk_f32 v178, v179, 0x3d000000, v11
	v_exp_f32_e32 v63, v63
	v_mul_f32_e32 v178, 0xbfb8aa3b, v178
	v_exp_f32_e32 v178, v178
	v_fmamk_f32 v181, v181, 0x3d000000, v13
	v_add_f32_e32 v63, 1.0, v63
	v_rcp_f32_e32 v179, v63
	v_add_f32_e32 v63, 1.0, v178
	v_rcp_f32_e32 v186, v63
	v_fmamk_f32 v63, v184, 0x3d000000, v16
	v_mul_f32_e32 v63, 0xbfb8aa3b, v63
	v_fmamk_f32 v178, v180, 0x3d000000, v12
	v_exp_f32_e32 v63, v63
	v_mul_f32_e32 v178, 0xbfb8aa3b, v178
	v_exp_f32_e32 v178, v178
	v_mul_f32_e32 v181, 0xbfb8aa3b, v181
	v_add_f32_e32 v63, 1.0, v63
	v_rcp_f32_e32 v180, v63
	v_add_f32_e32 v63, 1.0, v178
	v_fmamk_f32 v178, v185, 0x3d000000, v17
	v_mul_f32_e32 v178, 0xbfb8aa3b, v178
	v_exp_f32_e32 v178, v178
	v_exp_f32_e32 v181, v181
	v_mov_b32_e32 v61, v64
	s_nop 1
	v_permlane16_swap_b32_e32 v62, v61
	v_add_f32_e32 v178, 1.0, v178
	v_rcp_f32_e32 v183, v178
	v_cvt_f32_ubyte0_e32 v64, v62
	v_fmamk_f32 v65, v190, 0x3d000000, v6
	v_cvt_f32_ubyte1_e32 v228, v62
	v_fmamk_f32 v229, v191, 0x3d000000, v7
	v_add_f32_e32 v178, 1.0, v181
	v_pk_mul_f32 v[64:65], v[64:65], v[212:213]
	v_mov_b32_e32 v213, v179
	v_cvt_f32_ubyte2_e32 v230, v62
	v_fmamk_f32 v231, v192, 0x3d000000, v8
	v_fmamk_f32 v237, v188, 0x3d000000, v4
	v_rcp_f32_e32 v188, v178
	v_pk_mul_f32 v[178:179], v[228:229], v[212:213]
	v_mov_b32_e32 v213, v180
	v_cvt_f32_ubyte3_e32 v62, v62
	v_fmamk_f32 v235, v187, 0x3d000000, v3
	v_rcp_f32_e32 v187, v63
	v_fmamk_f32 v63, v193, 0x3d000000, v9
	v_pk_mul_f32 v[180:181], v[230:231], v[212:213]
	v_mov_b32_e32 v213, v183
	s_waitcnt vmcnt(10)
;     __device__ __forceinline__ void operator()(EPI_ARGS) const {
;     ...
;             for (int mp = 0; mp < 2; ++mp) { unsigned px[2], py[2]; unsigned gq[2][2] = {{0u, 0u}, {0u, 0u}};
;                 if (GATE_FP8) unpair16(glq[ai][mp], gq[0][0], gq[0][1], gq[1][0], gq[1][1]);
; #pragma unroll
;                 for (int h = 0; h < 2; ++h) { const int m = 2 * mp + h; const int row = u.pm * 256 + ai * 128 + wr * 64 + m * 16 + fr; const size_t off = (size_t)row * D + j0;
;                     const u32x4 yp = ypq[ai][mp][h]; float gsf[8];
;                     if (GATE_FP8) { v2u g8; g8.x = gq[h][0]; g8.y = gq[h][1]; const float k255 = 1.0f / 255.0f;
;                         gsf[0] = (float)(g8.x & 0xffu) * k255; gsf[1] = (float)((g8.x >> 8) & 0xffu) * k255; gsf[2] = (float)((g8.x >> 16) & 0xffu) * k255; gsf[3] = (float)(g8.x >> 24) * k255;
;                         gsf[4] = (float)(g8.y & 0xffu) * k255; gsf[5] = (float)((g8.y >> 8) & 0xffu) * k255; gsf[6] = (float)((g8.y >> 16) & 0xffu) * k255; gsf[7] = (float)(g8.y >> 24) * k255; }
;                     else { const u32x4 gs = *(const u32x4*)(SGS + off); gsf[0] = bf_lo(gs.x); gsf[1] = bf_hi(gs.x); gsf[2] = bf_lo(gs.y); gsf[3] = bf_hi(gs.y); gsf[4] = bf_lo(gs.z); gsf[5] = bf_hi(gs.z); gsf[6] = bf_lo(gs.w); gsf[7] = bf_hi(gs.w); }
;                     const f32x4 a0 = acc[ai][0][m][0] * asc + ba0, a1 = acc[ai][0][m][1] * asc + ba1, b0 = acc[ai][1][m][0] * asc + bb0, b1 = acc[ai][1][m][1] * asc + bb1;
;                     float o[8];
; #pragma unroll
;                     for (int j = 0; j < 4; ++j) { o[j] = a0[j] * sigmoidf_(b0[j]); o[4 + j] = a1[j] * sigmoidf_(b1[j]); }
;                     float mo[8] = {bf_lo(yp.x) + gsf[0] * o[0], bf_hi(yp.x) + gsf[1] * o[1], bf_lo(yp.y) + gsf[2] * o[2], bf_hi(yp.y) + gsf[3] * o[3],
;                                    bf_lo(yp.z) + gsf[4] * o[4], bf_hi(yp.z) + gsf[5] * o[5], bf_lo(yp.w) + gsf[6] * o[6], bf_hi(yp.w) + gsf[7] * o[7]};
;                     if (OUT_FP8) { px[h] = pk4_fp8(mo[0], mo[1], mo[2], mo[3]); py[h] = pk4_fp8(mo[4], mo[5], mo[6], mo[7]); }
;                     else { u32x4 w; w.x = cvt_pk_bf16(mo[0], mo[1]); w.y = cvt_pk_bf16(mo[2], mo[3]); w.z = cvt_pk_bf16(mo[4], mo[5]); w.w = cvt_pk_bf16(mo[6], mo[7]); *(u32x4*)(MG + off) = w; } }
;                 if (OUT_FP8) { const u32x4 q = pair16(px[0], py[0], px[1], py[1]);
	v_lshlrev_b32_e32 v190, 16, v214
	v_pk_mul_f32 v[62:63], v[62:63], v[212:213]
	v_mov_b32_e32 v213, v182
	v_fmac_f32_e32 v190, v64, v65
	v_and_b32_e32 v64, 0xffff0000, v214
	v_pk_mul_f32 v[182:183], v[232:233], v[212:213]
	v_mov_b32_e32 v213, v186
	v_fmac_f32_e32 v64, v178, v179
	v_and_b32_e32 v178, 0xffff0000, v215
	v_pk_mul_f32 v[184:185], v[234:235], v[212:213]
	v_fmac_f32_e32 v178, v62, v63
	v_lshlrev_b32_e32 v63, 16, v216
	v_and_b32_e32 v179, 0xffff0000, v216
	v_fmac_f32_e32 v63, v182, v183
	v_fmac_f32_e32 v179, v184, v185
	v_med3_f32 v182, v190, s74, v227
	v_med3_f32 v64, v64, s74, v227
	v_mov_b32_e32 v62, 0
	v_fmamk_f32 v163, v163, 0x3d000000, v11
	v_mov_b32_e32 v213, v187
	v_cvt_pk_fp8_f32 v62, v182, v64
	v_med3_f32 v64, v63, s74, v227
	v_med3_f32 v179, v179, s74, v227
	v_mov_b32_e32 v63, 0
	v_mul_f32_e32 v163, 0xbfb8aa3b, v163
	v_fmamk_f32 v239, v189, 0x3d000000, v5
	v_pk_mul_f32 v[186:187], v[236:237], v[212:213]
	v_mov_b32_e32 v213, v188
	v_lshlrev_b32_e32 v65, 16, v215
	v_cvt_pk_fp8_f32 v63, v64, v179
	v_exp_f32_e32 v163, v163
	v_pk_mul_f32 v[188:189], v[238:239], v[212:213]
	v_fmac_f32_e32 v65, v180, v181
	v_lshlrev_b32_e32 v180, 16, v217
	v_and_b32_e32 v181, 0xffff0000, v217
	v_fmac_f32_e32 v180, v186, v187
	v_fmac_f32_e32 v181, v188, v189
	v_med3_f32 v65, v65, s74, v227
	v_med3_f32 v178, v178, s74, v227
	v_cvt_pk_fp8_f32 v62, v65, v178 op_sel:[0,0,1]
	v_med3_f32 v64, v180, s74, v227
	v_med3_f32 v65, v181, s74, v227
	v_cvt_pk_fp8_f32 v63, v64, v65 op_sel:[0,0,1]
	v_cvt_f32_ubyte0_e32 v64, v61
	v_cvt_f32_ubyte1_e32 v178, v61
	v_cvt_f32_ubyte2_e32 v180, v61
	v_cvt_f32_ubyte3_e32 v182, v61
	v_fmamk_f32 v61, v166, 0x3d000000, v14
	v_add_f32_e32 v163, 1.0, v163
	v_mul_f32_e32 v61, 0xbfb8aa3b, v61
	v_fmamk_f32 v162, v162, 0x3d000000, v10
	v_fmamk_f32 v185, v170, 0x3d000000, v2
	v_rcp_f32_e32 v170, v163
	v_fmamk_f32 v163, v168, 0x3d000000, v16
	v_exp_f32_e32 v61, v61
	v_mul_f32_e32 v162, 0xbfb8aa3b, v162
	v_mul_f32_e32 v163, 0xbfb8aa3b, v163
	v_fmamk_f32 v164, v164, 0x3d000000, v12
	v_exp_f32_e32 v162, v162
	v_exp_f32_e32 v163, v163
	v_mul_f32_e32 v164, 0xbfb8aa3b, v164
	v_exp_f32_e32 v164, v164
	v_add_f32_e32 v61, 1.0, v61
	v_rcp_f32_e32 v213, v61
	v_add_f32_e32 v61, 1.0, v162
	v_fmamk_f32 v162, v167, 0x3d000000, v15
	v_add_f32_e32 v163, 1.0, v163
	v_mul_f32_e32 v162, 0xbfb8aa3b, v162
	v_rcp_f32_e32 v166, v163
	v_add_f32_e32 v163, 1.0, v164
	v_exp_f32_e32 v162, v162
	v_fmamk_f32 v189, v172, 0x3d000000, v4
	v_rcp_f32_e32 v172, v163
	v_fmamk_f32 v163, v169, 0x3d000000, v17
	v_mul_f32_e32 v163, 0xbfb8aa3b, v163
	v_exp_f32_e32 v163, v163
	v_fmamk_f32 v164, v165, 0x3d000000, v13
	v_add_f32_e32 v162, 1.0, v162
	v_mul_f32_e32 v164, 0xbfb8aa3b, v164
	v_rcp_f32_e32 v162, v162
	v_exp_f32_e32 v164, v164
	v_add_f32_e32 v163, 1.0, v163
	v_rcp_f32_e32 v167, v163
	v_fmamk_f32 v65, v174, 0x3d000000, v6
	v_rcp_f32_e32 v61, v61
	v_fmamk_f32 v179, v175, 0x3d000000, v7
	v_add_f32_e32 v163, 1.0, v164
	v_pk_mul_f32 v[64:65], v[64:65], v[212:213]
	v_mov_b32_e32 v213, v162
	v_fmamk_f32 v181, v176, 0x3d000000, v8
	v_rcp_f32_e32 v174, v163
	v_pk_mul_f32 v[162:163], v[178:179], v[212:213]
	v_mov_b32_e32 v213, v166
	v_fmamk_f32 v183, v177, 0x3d000000, v9
	v_pk_mul_f32 v[164:165], v[180:181], v[212:213]
	v_mov_b32_e32 v213, v167
	v_cvt_f32_ubyte0_e32 v184, v240
	v_pk_mul_f32 v[166:167], v[182:183], v[212:213]
	v_mov_b32_e32 v213, v61
	s_waitcnt vmcnt(9)
	v_lshlrev_b32_e32 v61, 16, v54
	v_cvt_f32_ubyte1_e32 v186, v240
	v_fmamk_f32 v187, v171, 0x3d000000, v3
	v_pk_mul_f32 v[168:169], v[184:185], v[212:213]
	v_mov_b32_e32 v213, v170
	v_fmac_f32_e32 v61, v64, v65
	v_and_b32_e32 v54, 0xffff0000, v54
	v_lshlrev_b32_e32 v64, 16, v55
	v_pk_mul_f32 v[170:171], v[186:187], v[212:213]
	v_fmac_f32_e32 v54, v162, v163
	v_fmac_f32_e32 v64, v164, v165
	v_lshlrev_b32_e32 v65, 16, v56
	v_and_b32_e32 v56, 0xffff0000, v56
	v_fmac_f32_e32 v65, v168, v169
	v_fmac_f32_e32 v56, v170, v171
	v_med3_f32 v61, v61, s74, v227
	v_med3_f32 v54, v54, s74, v227
	v_med3_f32 v163, v64, s74, v227
	v_mov_b32_e32 v64, 0
	v_cvt_f32_ubyte2_e32 v188, v240
	v_mov_b32_e32 v213, v172
	v_cvt_pk_fp8_f32 v64, v61, v54
	v_med3_f32 v54, v65, s74, v227
	v_med3_f32 v56, v56, s74, v227
	v_mov_b32_e32 v65, 0
	v_cvt_f32_ubyte3_e32 v190, v240
	v_fmamk_f32 v191, v173, 0x3d000000, v5
	v_pk_mul_f32 v[172:173], v[188:189], v[212:213]
	v_mov_b32_e32 v213, v174
	v_and_b32_e32 v55, 0xffff0000, v55
	v_cvt_pk_fp8_f32 v65, v54, v56
	v_pk_mul_f32 v[174:175], v[190:191], v[212:213]
	v_fmac_f32_e32 v55, v166, v167
	v_lshlrev_b32_e32 v162, 16, v57
	v_and_b32_e32 v57, 0xffff0000, v57
	v_fmac_f32_e32 v162, v172, v173
	v_fmac_f32_e32 v57, v174, v175
	v_med3_f32 v55, v55, s74, v227
	v_cvt_pk_fp8_f32 v64, v163, v55 op_sel:[0,0,1]
	v_med3_f32 v54, v162, s74, v227
	v_med3_f32 v55, v57, s74, v227
	v_cvt_pk_fp8_f32 v65, v54, v55 op_sel:[0,0,1]
	v_ashrrev_i32_e32 v61, 31, v60
	v_lshlrev_b64 v[54:55], 11, v[60:61]
	v_lshl_add_u64 v[54:55], s[16:17], 0, v[54:55]
	s_waitcnt vmcnt(8)
;     __device__ __forceinline__ void operator()(EPI_ARGS) const {
;     ...
;             for (int mp = 0; mp < 2; ++mp) { unsigned px[2], py[2]; unsigned gq[2][2] = {{0u, 0u}, {0u, 0u}};
;                 if (GATE_FP8) unpair16(glq[ai][mp], gq[0][0], gq[0][1], gq[1][0], gq[1][1]);
; #pragma unroll
;                 for (int h = 0; h < 2; ++h) { const int m = 2 * mp + h; const int row = u.pm * 256 + ai * 128 + wr * 64 + m * 16 + fr; const size_t off = (size_t)row * D + j0;
;                     const u32x4 yp = ypq[ai][mp][h]; float gsf[8];
;                     if (GATE_FP8) { v2u g8; g8.x = gq[h][0]; g8.y = gq[h][1]; const float k255 = 1.0f / 255.0f;
;                         gsf[0] = (float)(g8.x & 0xffu) * k255; gsf[1] = (float)((g8.x >> 8) & 0xffu) * k255; gsf[2] = (float)((g8.x >> 16) & 0xffu) * k255; gsf[3] = (float)(g8.x >> 24) * k255;
;                         gsf[4] = (float)(g8.y & 0xffu) * k255; gsf[5] = (float)((g8.y >> 8) & 0xffu) * k255; gsf[6] = (float)((g8.y >> 16) & 0xffu) * k255; gsf[7] = (float)(g8.y >> 24) * k255; }
;                     else { const u32x4 gs = *(const u32x4*)(SGS + off); gsf[0] = bf_lo(gs.x); gsf[1] = bf_hi(gs.x); gsf[2] = bf_lo(gs.y); gsf[3] = bf_hi(gs.y); gsf[4] = bf_lo(gs.z); gsf[5] = bf_hi(gs.z); gsf[6] = bf_lo(gs.w); gsf[7] = bf_hi(gs.w); }
;                     const f32x4 a0 = acc[ai][0][m][0] * asc + ba0, a1 = acc[ai][0][m][1] * asc + ba1, b0 = acc[ai][1][m][0] * asc + bb0, b1 = acc[ai][1][m][1] * asc + bb1;
;                     float o[8];
; #pragma unroll
;                     for (int j = 0; j < 4; ++j) { o[j] = a0[j] * sigmoidf_(b0[j]); o[4 + j] = a1[j] * sigmoidf_(b1[j]); }
;                     float mo[8] = {bf_lo(yp.x) + gsf[0] * o[0], bf_hi(yp.x) + gsf[1] * o[1], bf_lo(yp.y) + gsf[2] * o[2], bf_hi(yp.y) + gsf[3] * o[3],
;                                    bf_lo(yp.z) + gsf[4] * o[4], bf_hi(yp.z) + gsf[5] * o[5], bf_lo(yp.w) + gsf[6] * o[6], bf_hi(yp.w) + gsf[7] * o[7]};
;                     if (OUT_FP8) { px[h] = pk4_fp8(mo[0], mo[1], mo[2], mo[3]); py[h] = pk4_fp8(mo[4], mo[5], mo[6], mo[7]); }
;                     else { u32x4 w; w.x = cvt_pk_bf16(mo[0], mo[1]); w.y = cvt_pk_bf16(mo[2], mo[3]); w.z = cvt_pk_bf16(mo[4], mo[5]); w.w = cvt_pk_bf16(mo[6], mo[7]); *(u32x4*)(MG + off) = w; } }
;                 if (OUT_FP8) { const u32x4 q = pair16(px[0], py[0], px[1], py[1]);
	v_mov_b32_e32 v61, v52
	v_permlane16_swap_b32_e32 v62, v64
	v_permlane16_swap_b32_e32 v63, v65
	v_lshl_add_u64 v[54:55], v[54:55], 0, v[58:59]
	v_permlane16_swap_b32_e32 v50, v61
	global_store_dwordx4 v[54:55], v[62:65], off
	v_mov_b32_e32 v166, v53
	v_cvt_f32_ubyte0_e32 v53, v50
	v_cvt_f32_ubyte1_e32 v55, v50
	v_cvt_f32_ubyte2_e32 v57, v50
	v_cvt_f32_ubyte3_e32 v63, v50
	v_fmamk_f32 v50, v150, 0x3d000000, v14
	v_mul_f32_e32 v50, 0xbfb8aa3b, v50
	v_fmamk_f32 v54, v146, 0x3d000000, v10
	v_exp_f32_e32 v50, v50
	v_mul_f32_e32 v54, 0xbfb8aa3b, v54
	v_exp_f32_e32 v54, v54
	v_fmamk_f32 v56, v147, 0x3d000000, v11
	v_add_f32_e32 v50, 1.0, v50
	v_rcp_f32_e32 v146, v50
	v_add_f32_e32 v50, 1.0, v54
	v_rcp_f32_e32 v150, v50
	v_fmamk_f32 v50, v151, 0x3d000000, v15
	v_mul_f32_e32 v50, 0xbfb8aa3b, v50
	v_exp_f32_e32 v50, v50
	v_mul_f32_e32 v56, 0xbfb8aa3b, v56
	v_exp_f32_e32 v56, v56
	v_fmamk_f32 v64, v154, 0x3d000000, v2
	v_add_f32_e32 v50, 1.0, v50
	v_rcp_f32_e32 v154, v50
	v_add_f32_e32 v50, 1.0, v56
	v_fmamk_f32 v52, v158, 0x3d000000, v6
	v_rcp_f32_e32 v158, v50
	v_fmamk_f32 v50, v152, 0x3d000000, v16
	v_mul_f32_e32 v50, 0xbfb8aa3b, v50
	v_fmamk_f32 v62, v148, 0x3d000000, v12
	v_exp_f32_e32 v50, v50
	v_mul_f32_e32 v62, 0xbfb8aa3b, v62
	v_exp_f32_e32 v62, v62
	v_fmamk_f32 v147, v149, 0x3d000000, v13
	v_add_f32_e32 v50, 1.0, v50
	v_rcp_f32_e32 v148, v50
	v_add_f32_e32 v50, 1.0, v62
	v_mul_f32_e32 v147, 0xbfb8aa3b, v147
	v_rcp_f32_e32 v152, v50
	v_fmamk_f32 v50, v153, 0x3d000000, v17
	v_exp_f32_e32 v147, v147
	v_mul_f32_e32 v50, 0xbfb8aa3b, v50
	v_exp_f32_e32 v50, v50
	v_fmamk_f32 v56, v160, 0x3d000000, v8
	v_add_f32_e32 v147, 1.0, v147
	v_rcp_f32_e32 v160, v147
	v_permlane16_swap_b32_e32 v51, v166
	v_add_f32_e32 v50, 1.0, v50
	v_cvt_f32_ubyte0_e32 v65, v51
	v_fmamk_f32 v54, v159, 0x3d000000, v7
	v_fmamk_f32 v162, v155, 0x3d000000, v3
	v_fmamk_f32 v164, v156, 0x3d000000, v4
	v_rcp_f32_e32 v156, v50
	v_mov_b32_e32 v147, v212
	v_mov_b32_e32 v155, v212
	v_mov_b32_e32 v151, v212
	v_cvt_f32_ubyte1_e32 v163, v51
	v_cvt_f32_ubyte2_e32 v165, v51
	v_cvt_f32_ubyte3_e32 v51, v51
	v_fmamk_f32 v62, v161, 0x3d000000, v9
	v_fmamk_f32 v50, v157, 0x3d000000, v5
	v_pk_mul_f32 v[52:53], v[52:53], v[146:147]
	v_pk_mul_f32 v[54:55], v[54:55], v[154:155]
	v_pk_mul_f32 v[64:65], v[64:65], v[150:151]
	v_mov_b32_e32 v161, v212
	s_waitcnt vmcnt(7)
	v_lshlrev_b32_e32 v150, 16, v46
	v_and_b32_e32 v46, 0xffff0000, v46
	v_pk_mul_f32 v[50:51], v[50:51], v[160:161]
	v_fmac_f32_e32 v150, v52, v53
	v_fmac_f32_e32 v46, v54, v55
	v_lshlrev_b32_e32 v54, 16, v49
	v_and_b32_e32 v49, 0xffff0000, v49
	v_mov_b32_e32 v157, v212
	v_mov_b32_e32 v159, v212
	v_fmac_f32_e32 v49, v50, v51
	v_med3_f32 v50, v150, s74, v227
	v_med3_f32 v51, v46, s74, v227
	v_mov_b32_e32 v46, 0
	v_mov_b32_e32 v149, v212
	v_pk_mul_f32 v[62:63], v[62:63], v[156:157]
	v_pk_mul_f32 v[146:147], v[162:163], v[158:159]
	v_lshlrev_b32_e32 v52, 16, v47
	v_and_b32_e32 v47, 0xffff0000, v47
	v_lshlrev_b32_e32 v53, 16, v48
	v_and_b32_e32 v48, 0xffff0000, v48
	v_cvt_pk_fp8_f32 v46, v50, v51
	v_pk_mul_f32 v[56:57], v[56:57], v[148:149]
	v_fmac_f32_e32 v47, v62, v63
	v_fmac_f32_e32 v53, v64, v65
	v_fmac_f32_e32 v48, v146, v147
	v_fmac_f32_e32 v52, v56, v57
	v_med3_f32 v55, v47, s74, v227
	v_med3_f32 v50, v53, s74, v227
	v_med3_f32 v48, v48, s74, v227
	v_mov_b32_e32 v47, 0
	v_med3_f32 v52, v52, s74, v227
	v_cvt_pk_fp8_f32 v47, v50, v48
	v_fmamk_f32 v50, v134, 0x3d000000, v14
	v_cvt_pk_fp8_f32 v46, v52, v55 op_sel:[0,0,1]
	v_mul_f32_e32 v50, 0xbfb8aa3b, v50
	v_fmamk_f32 v52, v130, 0x3d000000, v10
	v_exp_f32_e32 v50, v50
	v_mul_f32_e32 v52, 0xbfb8aa3b, v52
	v_exp_f32_e32 v52, v52
	v_mov_b32_e32 v153, v212
	v_pk_mul_f32 v[148:149], v[164:165], v[152:153]
	v_add_f32_e32 v50, 1.0, v50
	v_fmac_f32_e32 v54, v148, v149
	v_rcp_f32_e32 v130, v50
	v_add_f32_e32 v50, 1.0, v52
	v_fmamk_f32 v52, v135, 0x3d000000, v15
	v_med3_f32 v48, v54, s74, v227
	v_mul_f32_e32 v52, 0xbfb8aa3b, v52
	v_fmamk_f32 v54, v131, 0x3d000000, v11
	v_exp_f32_e32 v52, v52
	v_mul_f32_e32 v54, 0xbfb8aa3b, v54
	v_exp_f32_e32 v54, v54
	v_med3_f32 v49, v49, s74, v227
	v_add_f32_e32 v52, 1.0, v52
	v_fmamk_f32 v56, v138, 0x3d000000, v2
	v_rcp_f32_e32 v138, v52
	v_add_f32_e32 v52, 1.0, v54
	v_fmamk_f32 v54, v136, 0x3d000000, v16
	v_cvt_pk_fp8_f32 v47, v48, v49 op_sel:[0,0,1]
	v_cvt_f32_ubyte0_e32 v49, v61
	v_cvt_f32_ubyte1_e32 v51, v61
	v_cvt_f32_ubyte2_e32 v53, v61
	v_cvt_f32_ubyte3_e32 v55, v61
	v_mul_f32_e32 v54, 0xbfb8aa3b, v54
	v_fmamk_f32 v61, v132, 0x3d000000, v12
	v_exp_f32_e32 v54, v54
	v_mul_f32_e32 v61, 0xbfb8aa3b, v61
	v_exp_f32_e32 v61, v61
	v_fmamk_f32 v131, v133, 0x3d000000, v13
	v_add_f32_e32 v54, 1.0, v54
	v_rcp_f32_e32 v132, v54
	v_add_f32_e32 v54, 1.0, v61
	v_fmamk_f32 v61, v137, 0x3d000000, v17
	v_mul_f32_e32 v61, 0xbfb8aa3b, v61
	v_exp_f32_e32 v61, v61
	v_mul_f32_e32 v131, 0xbfb8aa3b, v131
	v_exp_f32_e32 v131, v131
	v_fmamk_f32 v48, v142, 0x3d000000, v6
	v_rcp_f32_e32 v134, v50
	v_rcp_f32_e32 v142, v52
	v_add_f32_e32 v61, 1.0, v61
	v_fmamk_f32 v64, v140, 0x3d000000, v4
	v_rcp_f32_e32 v140, v61
	v_add_f32_e32 v61, 1.0, v131
	v_mov_b32_e32 v131, v212
	v_fmamk_f32 v50, v143, 0x3d000000, v7
	v_fmamk_f32 v62, v139, 0x3d000000, v3
	v_fmamk_f32 v52, v144, 0x3d000000, v8
	v_rcp_f32_e32 v144, v61
	v_pk_mul_f32 v[48:49], v[48:49], v[130:131]
	v_mov_b32_e32 v139, v212
	v_mov_b32_e32 v133, v212
	s_waitcnt vmcnt(6)
;     __device__ __forceinline__ void operator()(EPI_ARGS) const {
;     ...
;             for (int mp = 0; mp < 2; ++mp) { unsigned px[2], py[2]; unsigned gq[2][2] = {{0u, 0u}, {0u, 0u}};
;                 if (GATE_FP8) unpair16(glq[ai][mp], gq[0][0], gq[0][1], gq[1][0], gq[1][1]);
; #pragma unroll
;                 for (int h = 0; h < 2; ++h) { const int m = 2 * mp + h; const int row = u.pm * 256 + ai * 128 + wr * 64 + m * 16 + fr; const size_t off = (size_t)row * D + j0;
;                     const u32x4 yp = ypq[ai][mp][h]; float gsf[8];
;                     if (GATE_FP8) { v2u g8; g8.x = gq[h][0]; g8.y = gq[h][1]; const float k255 = 1.0f / 255.0f;
;                         gsf[0] = (float)(g8.x & 0xffu) * k255; gsf[1] = (float)((g8.x >> 8) & 0xffu) * k255; gsf[2] = (float)((g8.x >> 16) & 0xffu) * k255; gsf[3] = (float)(g8.x >> 24) * k255;
;                         gsf[4] = (float)(g8.y & 0xffu) * k255; gsf[5] = (float)((g8.y >> 8) & 0xffu) * k255; gsf[6] = (float)((g8.y >> 16) & 0xffu) * k255; gsf[7] = (float)(g8.y >> 24) * k255; }
;                     else { const u32x4 gs = *(const u32x4*)(SGS + off); gsf[0] = bf_lo(gs.x); gsf[1] = bf_hi(gs.x); gsf[2] = bf_lo(gs.y); gsf[3] = bf_hi(gs.y); gsf[4] = bf_lo(gs.z); gsf[5] = bf_hi(gs.z); gsf[6] = bf_lo(gs.w); gsf[7] = bf_hi(gs.w); }
;                     const f32x4 a0 = acc[ai][0][m][0] * asc + ba0, a1 = acc[ai][0][m][1] * asc + ba1, b0 = acc[ai][1][m][0] * asc + bb0, b1 = acc[ai][1][m][1] * asc + bb1;
;                     float o[8];
; #pragma unroll
;                     for (int j = 0; j < 4; ++j) { o[j] = a0[j] * sigmoidf_(b0[j]); o[4 + j] = a1[j] * sigmoidf_(b1[j]); }
;                     float mo[8] = {bf_lo(yp.x) + gsf[0] * o[0], bf_hi(yp.x) + gsf[1] * o[1], bf_lo(yp.y) + gsf[2] * o[2], bf_hi(yp.y) + gsf[3] * o[3],
;                                    bf_lo(yp.z) + gsf[4] * o[4], bf_hi(yp.z) + gsf[5] * o[5], bf_lo(yp.w) + gsf[6] * o[6], bf_hi(yp.w) + gsf[7] * o[7]};
;                     if (OUT_FP8) { px[h] = pk4_fp8(mo[0], mo[1], mo[2], mo[3]); py[h] = pk4_fp8(mo[4], mo[5], mo[6], mo[7]); }
;                     else { u32x4 w; w.x = cvt_pk_bf16(mo[0], mo[1]); w.y = cvt_pk_bf16(mo[2], mo[3]); w.z = cvt_pk_bf16(mo[4], mo[5]); w.w = cvt_pk_bf16(mo[6], mo[7]); *(u32x4*)(MG + off) = w; } }
;                 if (OUT_FP8) { const u32x4 q = pair16(px[0], py[0], px[1], py[1]);
	v_lshlrev_b32_e32 v61, 16, v42
	v_cvt_f32_ubyte0_e32 v57, v166
	v_cvt_f32_ubyte1_e32 v63, v166
	v_pk_mul_f32 v[50:51], v[50:51], v[138:139]
	v_pk_mul_f32 v[52:53], v[52:53], v[132:133]
	v_mov_b32_e32 v135, v212
	v_mov_b32_e32 v143, v212
	v_fmac_f32_e32 v61, v48, v49
	v_and_b32_e32 v42, 0xffff0000, v42
	v_lshlrev_b32_e32 v48, 16, v43
	v_rcp_f32_e32 v136, v54
	v_pk_mul_f32 v[56:57], v[56:57], v[134:135]
	v_pk_mul_f32 v[62:63], v[62:63], v[142:143]
	v_fmac_f32_e32 v42, v50, v51
	v_fmac_f32_e32 v48, v52, v53
	v_lshlrev_b32_e32 v49, 16, v44
	v_and_b32_e32 v44, 0xffff0000, v44
	v_fmac_f32_e32 v49, v56, v57
	v_fmac_f32_e32 v44, v62, v63
	v_med3_f32 v51, v61, s74, v227
	v_med3_f32 v42, v42, s74, v227
	v_med3_f32 v52, v48, s74, v227
	v_mov_b32_e32 v48, 0
	v_fmamk_f32 v54, v145, 0x3d000000, v9
	v_fmamk_f32 v146, v141, 0x3d000000, v5
	v_mov_b32_e32 v141, v212
	v_cvt_pk_fp8_f32 v48, v51, v42
	v_med3_f32 v42, v49, s74, v227
	v_med3_f32 v44, v44, s74, v227
	v_mov_b32_e32 v49, 0
	v_cvt_f32_ubyte2_e32 v65, v166
	v_cvt_f32_ubyte3_e32 v147, v166
	v_pk_mul_f32 v[54:55], v[54:55], v[140:141]
	v_mov_b32_e32 v137, v212
	v_mov_b32_e32 v145, v212
	v_and_b32_e32 v43, 0xffff0000, v43
	v_cvt_pk_fp8_f32 v49, v42, v44
	v_pk_mul_f32 v[64:65], v[64:65], v[136:137]
	v_pk_mul_f32 v[130:131], v[146:147], v[144:145]
	v_fmac_f32_e32 v43, v54, v55
	v_lshlrev_b32_e32 v50, 16, v45
	v_and_b32_e32 v45, 0xffff0000, v45
	v_fmac_f32_e32 v50, v64, v65
	v_fmac_f32_e32 v45, v130, v131
	v_med3_f32 v43, v43, s74, v227
	v_cvt_pk_fp8_f32 v48, v52, v43 op_sel:[0,0,1]
	v_med3_f32 v42, v50, s74, v227
	v_med3_f32 v43, v45, s74, v227
	v_cvt_pk_fp8_f32 v49, v42, v43 op_sel:[0,0,1]
	v_or_b32_e32 v42, 32, v60
	v_ashrrev_i32_e32 v43, 31, v42
	v_lshlrev_b64 v[42:43], 11, v[42:43]
	v_lshl_add_u64 v[42:43], s[16:17], 0, v[42:43]
	v_permlane16_swap_b32_e32 v46, v48
	v_permlane16_swap_b32_e32 v47, v49
	v_lshl_add_u64 v[42:43], v[42:43], 0, v[58:59]
	global_store_dwordx4 v[42:43], v[46:49], off
	s_waitcnt vmcnt(5)
	v_mov_b32_e32 v43, v40
	s_nop 1
	v_permlane16_swap_b32_e32 v38, v43
	v_mov_b32_e32 v61, v41
	v_cvt_f32_ubyte0_e32 v41, v38
	v_cvt_f32_ubyte1_e32 v45, v38
	v_cvt_f32_ubyte2_e32 v47, v38
	v_cvt_f32_ubyte3_e32 v49, v38
	v_fmamk_f32 v38, v126, 0x3d000000, v14
	v_mul_f32_e32 v38, 0xbfb8aa3b, v38
	v_fmamk_f32 v44, v122, 0x3d000000, v10
	v_exp_f32_e32 v38, v38
	v_mul_f32_e32 v44, 0xbfb8aa3b, v44
	v_exp_f32_e32 v44, v44
	v_fmamk_f32 v46, v123, 0x3d000000, v11
	v_add_f32_e32 v38, 1.0, v38
	v_rcp_f32_e32 v56, v38
	v_add_f32_e32 v38, 1.0, v44
	v_rcp_f32_e32 v62, v38
	v_fmamk_f32 v38, v127, 0x3d000000, v15
	v_mul_f32_e32 v38, 0xbfb8aa3b, v38
	v_exp_f32_e32 v38, v38
	v_mul_f32_e32 v46, 0xbfb8aa3b, v46
	v_exp_f32_e32 v46, v46
	v_fmamk_f32 v50, v114, 0x3d000000, v2
	v_add_f32_e32 v38, 1.0, v38
	v_rcp_f32_e32 v64, v38
	v_add_f32_e32 v38, 1.0, v46
	v_rcp_f32_e32 v114, v38
	v_fmamk_f32 v38, v128, 0x3d000000, v16
	v_mul_f32_e32 v38, 0xbfb8aa3b, v38
	v_fmamk_f32 v48, v124, 0x3d000000, v12
	v_exp_f32_e32 v38, v38
	v_mul_f32_e32 v48, 0xbfb8aa3b, v48
	v_exp_f32_e32 v48, v48
	v_fmamk_f32 v57, v125, 0x3d000000, v13
	v_add_f32_e32 v38, 1.0, v38
	v_fmamk_f32 v40, v118, 0x3d000000, v6
	v_rcp_f32_e32 v118, v38
	v_add_f32_e32 v38, 1.0, v48
	v_mul_f32_e32 v57, 0xbfb8aa3b, v57
	v_fmamk_f32 v54, v116, 0x3d000000, v4
	v_rcp_f32_e32 v116, v38
	v_fmamk_f32 v38, v129, 0x3d000000, v17
	v_exp_f32_e32 v57, v57
	v_mul_f32_e32 v38, 0xbfb8aa3b, v38
	v_exp_f32_e32 v38, v38
	v_permlane16_swap_b32_e32 v39, v61
	v_add_f32_e32 v57, 1.0, v57
	v_rcp_f32_e32 v122, v57
	v_add_f32_e32 v38, 1.0, v38
	v_fmamk_f32 v44, v119, 0x3d000000, v7
	v_fmamk_f32 v46, v120, 0x3d000000, v8
	v_rcp_f32_e32 v120, v38
	v_mov_b32_e32 v57, v212
	v_mov_b32_e32 v65, v212
	v_cvt_f32_ubyte0_e32 v51, v39
	v_cvt_f32_ubyte1_e32 v53, v39
	v_cvt_f32_ubyte2_e32 v55, v39
	v_cvt_f32_ubyte3_e32 v39, v39
	v_fmamk_f32 v38, v117, 0x3d000000, v5
	v_pk_mul_f32 v[40:41], v[40:41], v[56:57]
	v_pk_mul_f32 v[44:45], v[44:45], v[64:65]
	v_mov_b32_e32 v123, v212
	s_waitcnt vmcnt(4)
	v_lshlrev_b32_e32 v56, 16, v34
	v_and_b32_e32 v34, 0xffff0000, v34
	v_pk_mul_f32 v[38:39], v[38:39], v[122:123]
	v_fmac_f32_e32 v56, v40, v41
	v_fmac_f32_e32 v34, v44, v45
	v_lshlrev_b32_e32 v44, 16, v37
	v_and_b32_e32 v37, 0xffff0000, v37
	v_fmamk_f32 v52, v115, 0x3d000000, v3
	v_fmamk_f32 v48, v121, 0x3d000000, v9
	v_mov_b32_e32 v121, v212
	v_mov_b32_e32 v63, v212
	v_mov_b32_e32 v115, v212
	v_fmac_f32_e32 v37, v38, v39
	v_med3_f32 v38, v56, s74, v227
	v_med3_f32 v39, v34, s74, v227
	v_mov_b32_e32 v34, 0
	v_mov_b32_e32 v119, v212
	v_pk_mul_f32 v[48:49], v[48:49], v[120:121]
	v_pk_mul_f32 v[50:51], v[50:51], v[62:63]
	v_pk_mul_f32 v[52:53], v[52:53], v[114:115]
	v_lshlrev_b32_e32 v40, 16, v35
	v_and_b32_e32 v35, 0xffff0000, v35
	v_lshlrev_b32_e32 v41, 16, v36
	v_and_b32_e32 v36, 0xffff0000, v36
	v_cvt_pk_fp8_f32 v34, v38, v39
	v_pk_mul_f32 v[46:47], v[46:47], v[118:119]
	v_fmac_f32_e32 v35, v48, v49
	v_fmac_f32_e32 v41, v50, v51
	v_fmac_f32_e32 v36, v52, v53
	v_fmac_f32_e32 v40, v46, v47
	v_med3_f32 v45, v35, s74, v227
	v_med3_f32 v38, v41, s74, v227
	v_med3_f32 v36, v36, s74, v227
	v_mov_b32_e32 v35, 0
	v_med3_f32 v40, v40, s74, v227
	v_cvt_pk_fp8_f32 v35, v38, v36
	v_fmamk_f32 v38, v110, 0x3d000000, v14
	v_cvt_pk_fp8_f32 v34, v40, v45 op_sel:[0,0,1]
	v_mul_f32_e32 v38, 0xbfb8aa3b, v38
	v_fmamk_f32 v40, v106, 0x3d000000, v10
	v_exp_f32_e32 v38, v38
	v_mul_f32_e32 v40, 0xbfb8aa3b, v40
	v_exp_f32_e32 v40, v40
	v_mov_b32_e32 v117, v212
	v_pk_mul_f32 v[54:55], v[54:55], v[116:117]
	v_add_f32_e32 v38, 1.0, v38
	v_fmac_f32_e32 v44, v54, v55
	v_med3_f32 v36, v44, s74, v227
	v_med3_f32 v37, v37, s74, v227
;     __device__ __forceinline__ void operator()(EPI_ARGS) const {
;     ...
;             for (int mp = 0; mp < 2; ++mp) { unsigned px[2], py[2]; unsigned gq[2][2] = {{0u, 0u}, {0u, 0u}};
;                 if (GATE_FP8) unpair16(glq[ai][mp], gq[0][0], gq[0][1], gq[1][0], gq[1][1]);
; #pragma unroll
;                 for (int h = 0; h < 2; ++h) { const int m = 2 * mp + h; const int row = u.pm * 256 + ai * 128 + wr * 64 + m * 16 + fr; const size_t off = (size_t)row * D + j0;
;                     const u32x4 yp = ypq[ai][mp][h]; float gsf[8];
;                     if (GATE_FP8) { v2u g8; g8.x = gq[h][0]; g8.y = gq[h][1]; const float k255 = 1.0f / 255.0f;
;                         gsf[0] = (float)(g8.x & 0xffu) * k255; gsf[1] = (float)((g8.x >> 8) & 0xffu) * k255; gsf[2] = (float)((g8.x >> 16) & 0xffu) * k255; gsf[3] = (float)(g8.x >> 24) * k255;
;                         gsf[4] = (float)(g8.y & 0xffu) * k255; gsf[5] = (float)((g8.y >> 8) & 0xffu) * k255; gsf[6] = (float)((g8.y >> 16) & 0xffu) * k255; gsf[7] = (float)(g8.y >> 24) * k255; }
;                     else { const u32x4 gs = *(const u32x4*)(SGS + off); gsf[0] = bf_lo(gs.x); gsf[1] = bf_hi(gs.x); gsf[2] = bf_lo(gs.y); gsf[3] = bf_hi(gs.y); gsf[4] = bf_lo(gs.z); gsf[5] = bf_hi(gs.z); gsf[6] = bf_lo(gs.w); gsf[7] = bf_hi(gs.w); }
;                     const f32x4 a0 = acc[ai][0][m][0] * asc + ba0, a1 = acc[ai][0][m][1] * asc + ba1, b0 = acc[ai][1][m][0] * asc + bb0, b1 = acc[ai][1][m][1] * asc + bb1;
;                     float o[8];
; #pragma unroll
;                     for (int j = 0; j < 4; ++j) { o[j] = a0[j] * sigmoidf_(b0[j]); o[4 + j] = a1[j] * sigmoidf_(b1[j]); }
;                     float mo[8] = {bf_lo(yp.x) + gsf[0] * o[0], bf_hi(yp.x) + gsf[1] * o[1], bf_lo(yp.y) + gsf[2] * o[2], bf_hi(yp.y) + gsf[3] * o[3],
;                                    bf_lo(yp.z) + gsf[4] * o[4], bf_hi(yp.z) + gsf[5] * o[5], bf_lo(yp.w) + gsf[6] * o[6], bf_hi(yp.w) + gsf[7] * o[7]};
;                     if (OUT_FP8) { px[h] = pk4_fp8(mo[0], mo[1], mo[2], mo[3]); py[h] = pk4_fp8(mo[4], mo[5], mo[6], mo[7]); }
;                     else { u32x4 w; w.x = cvt_pk_bf16(mo[0], mo[1]); w.y = cvt_pk_bf16(mo[2], mo[3]); w.z = cvt_pk_bf16(mo[4], mo[5]); w.w = cvt_pk_bf16(mo[6], mo[7]); *(u32x4*)(MG + off) = w; } }
;                 if (OUT_FP8) { const u32x4 q = pair16(px[0], py[0], px[1], py[1]);
	v_rcp_f32_e32 v54, v38
	v_add_f32_e32 v38, 1.0, v40
	v_fmamk_f32 v40, v111, 0x3d000000, v15
	v_cvt_pk_fp8_f32 v35, v36, v37 op_sel:[0,0,1]
	v_cvt_f32_ubyte0_e32 v37, v43
	v_cvt_f32_ubyte1_e32 v39, v43
	v_cvt_f32_ubyte2_e32 v41, v43
	v_cvt_f32_ubyte3_e32 v45, v43
	v_mul_f32_e32 v40, 0xbfb8aa3b, v40
	v_fmamk_f32 v43, v107, 0x3d000000, v11
	v_exp_f32_e32 v40, v40
	v_mul_f32_e32 v43, 0xbfb8aa3b, v43
	v_exp_f32_e32 v43, v43
	v_fmamk_f32 v44, v108, 0x3d000000, v12
	v_add_f32_e32 v40, 1.0, v40
	v_rcp_f32_e32 v62, v40
	v_add_f32_e32 v40, 1.0, v43
	v_fmamk_f32 v43, v112, 0x3d000000, v16
	v_mul_f32_e32 v43, 0xbfb8aa3b, v43
	v_exp_f32_e32 v43, v43
	v_mul_f32_e32 v44, 0xbfb8aa3b, v44
	v_exp_f32_e32 v44, v44
	v_fmamk_f32 v46, v98, 0x3d000000, v2
	v_add_f32_e32 v43, 1.0, v43
	v_rcp_f32_e32 v98, v43
	v_add_f32_e32 v43, 1.0, v44
	v_fmamk_f32 v50, v100, 0x3d000000, v4
	v_rcp_f32_e32 v100, v43
	v_fmamk_f32 v43, v113, 0x3d000000, v17
	v_mul_f32_e32 v43, 0xbfb8aa3b, v43
	v_fmamk_f32 v52, v109, 0x3d000000, v13
	v_exp_f32_e32 v43, v43
	v_mul_f32_e32 v52, 0xbfb8aa3b, v52
	v_exp_f32_e32 v55, v52
	v_rcp_f32_e32 v56, v38
	v_rcp_f32_e32 v64, v40
	v_add_f32_e32 v43, 1.0, v43
	v_fmamk_f32 v36, v102, 0x3d000000, v6
	v_rcp_f32_e32 v102, v43
	v_add_f32_e32 v43, 1.0, v55
	v_mov_b32_e32 v55, v212
	v_fmamk_f32 v38, v103, 0x3d000000, v7
	v_fmamk_f32 v48, v99, 0x3d000000, v3
	v_fmamk_f32 v40, v104, 0x3d000000, v8
	v_rcp_f32_e32 v104, v43
	v_pk_mul_f32 v[36:37], v[36:37], v[54:55]
	v_mov_b32_e32 v99, v212
	s_waitcnt vmcnt(3)
	v_lshlrev_b32_e32 v43, 16, v30
	v_cvt_f32_ubyte0_e32 v47, v61
	v_cvt_f32_ubyte1_e32 v49, v61
	v_pk_mul_f32 v[38:39], v[38:39], v[62:63]
	v_pk_mul_f32 v[40:41], v[40:41], v[98:99]
	v_fmac_f32_e32 v43, v36, v37
	v_and_b32_e32 v30, 0xffff0000, v30
	v_lshlrev_b32_e32 v36, 16, v31
	v_pk_mul_f32 v[46:47], v[46:47], v[56:57]
	v_pk_mul_f32 v[48:49], v[48:49], v[64:65]
	v_fmac_f32_e32 v30, v38, v39
	v_fmac_f32_e32 v36, v40, v41
	v_lshlrev_b32_e32 v37, 16, v32
	v_and_b32_e32 v32, 0xffff0000, v32
	v_fmac_f32_e32 v37, v46, v47
	v_fmac_f32_e32 v32, v48, v49
	v_med3_f32 v39, v43, s74, v227
	v_med3_f32 v30, v30, s74, v227
	v_med3_f32 v40, v36, s74, v227
	v_mov_b32_e32 v36, 0
	v_fmamk_f32 v44, v105, 0x3d000000, v9
	v_mov_b32_e32 v103, v212
	v_cvt_pk_fp8_f32 v36, v39, v30
	v_med3_f32 v30, v37, s74, v227
	v_med3_f32 v32, v32, s74, v227
	v_mov_b32_e32 v37, 0
	v_cvt_f32_ubyte2_e32 v51, v61
	v_cvt_f32_ubyte3_e32 v53, v61
	v_fmamk_f32 v52, v101, 0x3d000000, v5
	v_pk_mul_f32 v[44:45], v[44:45], v[102:103]
	v_mov_b32_e32 v101, v212
	v_mov_b32_e32 v105, v212
	v_and_b32_e32 v31, 0xffff0000, v31
	v_cvt_pk_fp8_f32 v37, v30, v32
	v_pk_mul_f32 v[50:51], v[50:51], v[100:101]
	v_pk_mul_f32 v[52:53], v[52:53], v[104:105]
	v_fmac_f32_e32 v31, v44, v45
	v_lshlrev_b32_e32 v38, 16, v33
	v_and_b32_e32 v33, 0xffff0000, v33
	v_fmac_f32_e32 v38, v50, v51
	v_fmac_f32_e32 v33, v52, v53
	v_med3_f32 v31, v31, s74, v227
	v_cvt_pk_fp8_f32 v36, v40, v31 op_sel:[0,0,1]
	v_med3_f32 v30, v38, s74, v227
	v_med3_f32 v31, v33, s74, v227
	v_add_u32_e32 v42, 0x80, v60
	v_cvt_pk_fp8_f32 v37, v30, v31 op_sel:[0,0,1]
	v_ashrrev_i32_e32 v43, 31, v42
	v_lshlrev_b64 v[30:31], 11, v[42:43]
	v_lshl_add_u64 v[30:31], s[16:17], 0, v[30:31]
	s_waitcnt vmcnt(2)
	v_mov_b32_e32 v61, v28
	v_permlane16_swap_b32_e32 v34, v36
	v_permlane16_swap_b32_e32 v35, v37
	v_lshl_add_u64 v[30:31], v[30:31], 0, v[58:59]
	v_permlane16_swap_b32_e32 v26, v61
	global_store_dwordx4 v[30:31], v[34:37], off
	v_mov_b32_e32 v62, v29
	v_cvt_f32_ubyte0_e32 v29, v26
	v_cvt_f32_ubyte1_e32 v31, v26
	v_cvt_f32_ubyte2_e32 v33, v26
	v_cvt_f32_ubyte3_e32 v35, v26
	v_fmamk_f32 v26, v94, 0x3d000000, v14
	v_mul_f32_e32 v26, 0xbfb8aa3b, v26
	v_fmamk_f32 v30, v90, 0x3d000000, v10
	v_exp_f32_e32 v26, v26
	v_mul_f32_e32 v30, 0xbfb8aa3b, v30
	v_exp_f32_e32 v30, v30
	v_fmamk_f32 v32, v91, 0x3d000000, v11
	v_add_f32_e32 v26, 1.0, v26
	v_rcp_f32_e32 v42, v26
	v_add_f32_e32 v26, 1.0, v30
	v_rcp_f32_e32 v44, v26
	v_fmamk_f32 v26, v95, 0x3d000000, v15
	v_mul_f32_e32 v26, 0xbfb8aa3b, v26
	v_exp_f32_e32 v26, v26
	v_mul_f32_e32 v32, 0xbfb8aa3b, v32
	v_exp_f32_e32 v32, v32
	v_fmamk_f32 v34, v92, 0x3d000000, v12
	v_add_f32_e32 v26, 1.0, v26
	v_rcp_f32_e32 v46, v26
	v_add_f32_e32 v26, 1.0, v32
	v_rcp_f32_e32 v48, v26
	v_fmamk_f32 v26, v96, 0x3d000000, v16
	v_mul_f32_e32 v26, 0xbfb8aa3b, v26
	v_exp_f32_e32 v26, v26
	v_mul_f32_e32 v34, 0xbfb8aa3b, v34
	v_exp_f32_e32 v34, v34
	v_fmamk_f32 v43, v93, 0x3d000000, v13
	v_add_f32_e32 v26, 1.0, v26
	v_rcp_f32_e32 v50, v26
	v_add_f32_e32 v26, 1.0, v34
	v_rcp_f32_e32 v52, v26
	v_fmamk_f32 v26, v97, 0x3d000000, v17
	v_mul_f32_e32 v26, 0xbfb8aa3b, v26
	v_mul_f32_e32 v43, 0xbfb8aa3b, v43
	v_exp_f32_e32 v26, v26
	v_exp_f32_e32 v43, v43
	v_fmamk_f32 v10, v74, 0x3d000000, v10
	v_mul_f32_e32 v10, 0xbfb8aa3b, v10
	v_add_f32_e32 v26, 1.0, v26
	v_add_f32_e32 v43, 1.0, v43
	v_rcp_f32_e32 v54, v26
	v_rcp_f32_e32 v56, v43
	v_permlane16_swap_b32_e32 v27, v62
	v_fmamk_f32 v28, v86, 0x3d000000, v6
	v_fmamk_f32 v30, v87, 0x3d000000, v7
	v_mov_b32_e32 v43, v212
	v_mov_b32_e32 v47, v212
	v_exp_f32_e32 v10, v10
	v_cvt_f32_ubyte0_e32 v37, v27
	v_cvt_f32_ubyte1_e32 v39, v27
	v_cvt_f32_ubyte2_e32 v41, v27
	v_cvt_f32_ubyte3_e32 v27, v27
	v_fmamk_f32 v36, v82, 0x3d000000, v2
	v_fmamk_f32 v38, v83, 0x3d000000, v3
	v_fmamk_f32 v34, v89, 0x3d000000, v9
	v_fmamk_f32 v26, v85, 0x3d000000, v5
	v_pk_mul_f32 v[28:29], v[28:29], v[42:43]
	v_pk_mul_f32 v[30:31], v[30:31], v[46:47]
	v_mov_b32_e32 v45, v212
	v_mov_b32_e32 v49, v212
	s_waitcnt vmcnt(1)
;     __device__ __forceinline__ void operator()(EPI_ARGS) const {
;     ...
;             for (int mp = 0; mp < 2; ++mp) { unsigned px[2], py[2]; unsigned gq[2][2] = {{0u, 0u}, {0u, 0u}};
;                 if (GATE_FP8) unpair16(glq[ai][mp], gq[0][0], gq[0][1], gq[1][0], gq[1][1]);
; #pragma unroll
;                 for (int h = 0; h < 2; ++h) { const int m = 2 * mp + h; const int row = u.pm * 256 + ai * 128 + wr * 64 + m * 16 + fr; const size_t off = (size_t)row * D + j0;
;                     const u32x4 yp = ypq[ai][mp][h]; float gsf[8];
;                     if (GATE_FP8) { v2u g8; g8.x = gq[h][0]; g8.y = gq[h][1]; const float k255 = 1.0f / 255.0f;
;                         gsf[0] = (float)(g8.x & 0xffu) * k255; gsf[1] = (float)((g8.x >> 8) & 0xffu) * k255; gsf[2] = (float)((g8.x >> 16) & 0xffu) * k255; gsf[3] = (float)(g8.x >> 24) * k255;
;                         gsf[4] = (float)(g8.y & 0xffu) * k255; gsf[5] = (float)((g8.y >> 8) & 0xffu) * k255; gsf[6] = (float)((g8.y >> 16) & 0xffu) * k255; gsf[7] = (float)(g8.y >> 24) * k255; }
;                     else { const u32x4 gs = *(const u32x4*)(SGS + off); gsf[0] = bf_lo(gs.x); gsf[1] = bf_hi(gs.x); gsf[2] = bf_lo(gs.y); gsf[3] = bf_hi(gs.y); gsf[4] = bf_lo(gs.z); gsf[5] = bf_hi(gs.z); gsf[6] = bf_lo(gs.w); gsf[7] = bf_hi(gs.w); }
;                     const f32x4 a0 = acc[ai][0][m][0] * asc + ba0, a1 = acc[ai][0][m][1] * asc + ba1, b0 = acc[ai][1][m][0] * asc + bb0, b1 = acc[ai][1][m][1] * asc + bb1;
;                     float o[8];
; #pragma unroll
;                     for (int j = 0; j < 4; ++j) { o[j] = a0[j] * sigmoidf_(b0[j]); o[4 + j] = a1[j] * sigmoidf_(b1[j]); }
;                     float mo[8] = {bf_lo(yp.x) + gsf[0] * o[0], bf_hi(yp.x) + gsf[1] * o[1], bf_lo(yp.y) + gsf[2] * o[2], bf_hi(yp.y) + gsf[3] * o[3],
;                                    bf_lo(yp.z) + gsf[4] * o[4], bf_hi(yp.z) + gsf[5] * o[5], bf_lo(yp.w) + gsf[6] * o[6], bf_hi(yp.w) + gsf[7] * o[7]};
;                     if (OUT_FP8) { px[h] = pk4_fp8(mo[0], mo[1], mo[2], mo[3]); py[h] = pk4_fp8(mo[4], mo[5], mo[6], mo[7]); }
;                     else { u32x4 w; w.x = cvt_pk_bf16(mo[0], mo[1]); w.y = cvt_pk_bf16(mo[2], mo[3]); w.z = cvt_pk_bf16(mo[4], mo[5]); w.w = cvt_pk_bf16(mo[6], mo[7]); *(u32x4*)(MG + off) = w; } }
;                 if (OUT_FP8) { const u32x4 q = pair16(px[0], py[0], px[1], py[1]);
	v_lshlrev_b32_e32 v42, 16, v22
	v_and_b32_e32 v22, 0xffff0000, v22
	v_fmamk_f32 v32, v88, 0x3d000000, v8
	v_mov_b32_e32 v51, v212
	v_pk_mul_f32 v[34:35], v[34:35], v[54:55]
	v_pk_mul_f32 v[36:37], v[36:37], v[44:45]
	v_pk_mul_f32 v[38:39], v[38:39], v[48:49]
	v_pk_mul_f32 v[26:27], v[26:27], v[56:57]
	v_fmac_f32_e32 v42, v28, v29
	v_fmac_f32_e32 v22, v30, v31
	v_lshlrev_b32_e32 v28, 16, v23
	v_and_b32_e32 v23, 0xffff0000, v23
	v_lshlrev_b32_e32 v29, 16, v24
	v_and_b32_e32 v24, 0xffff0000, v24
	v_lshlrev_b32_e32 v30, 16, v25
	v_and_b32_e32 v25, 0xffff0000, v25
	v_pk_mul_f32 v[32:33], v[32:33], v[50:51]
	v_fmac_f32_e32 v23, v34, v35
	v_fmac_f32_e32 v29, v36, v37
	v_fmac_f32_e32 v24, v38, v39
	v_fmac_f32_e32 v25, v26, v27
	v_med3_f32 v26, v42, s74, v227
	v_med3_f32 v27, v22, s74, v227
	v_mov_b32_e32 v22, 0
	v_fmac_f32_e32 v28, v32, v33
	v_med3_f32 v31, v23, s74, v227
	v_cvt_pk_fp8_f32 v22, v26, v27
	v_med3_f32 v26, v29, s74, v227
	v_med3_f32 v24, v24, s74, v227
	v_mov_b32_e32 v23, 0
	v_fmamk_f32 v32, v66, 0x3d000000, v2
	v_add_f32_e32 v2, 1.0, v10
	v_fmamk_f32 v10, v75, 0x3d000000, v11
	v_cvt_pk_fp8_f32 v23, v26, v24
	v_fmamk_f32 v26, v71, 0x3d000000, v7
	v_fmamk_f32 v7, v79, 0x3d000000, v15
	v_mul_f32_e32 v10, 0xbfb8aa3b, v10
	v_mul_f32_e32 v7, 0xbfb8aa3b, v7
	v_exp_f32_e32 v11, v10
	v_fmamk_f32 v40, v84, 0x3d000000, v4
	v_mov_b32_e32 v53, v212
	v_exp_f32_e32 v7, v7
	v_pk_mul_f32 v[40:41], v[40:41], v[52:53]
	v_med3_f32 v25, v25, s74, v227
	v_fmac_f32_e32 v30, v40, v41
	v_med3_f32 v24, v30, s74, v227
	v_fmamk_f32 v34, v67, 0x3d000000, v3
	v_add_f32_e32 v3, 1.0, v11
	v_cvt_pk_fp8_f32 v23, v24, v25 op_sel:[0,0,1]
	v_fmamk_f32 v24, v70, 0x3d000000, v6
	v_fmamk_f32 v6, v78, 0x3d000000, v14
	v_add_f32_e32 v7, 1.0, v7
	v_rcp_f32_e32 v14, v3
	v_fmamk_f32 v3, v80, 0x3d000000, v16
	v_rcp_f32_e32 v10, v7
	v_mul_f32_e32 v3, 0xbfb8aa3b, v3
	v_fmamk_f32 v7, v76, 0x3d000000, v12
	v_exp_f32_e32 v3, v3
	v_mul_f32_e32 v7, 0xbfb8aa3b, v7
	v_exp_f32_e32 v7, v7
	v_mul_f32_e32 v6, 0xbfb8aa3b, v6
	v_exp_f32_e32 v6, v6
	v_add_f32_e32 v3, 1.0, v3
	v_med3_f32 v28, v28, s74, v227
	v_rcp_f32_e32 v12, v3
	v_add_f32_e32 v3, 1.0, v7
	v_fmac_f32_e32 v17, 0x3d000000, v81
	v_cvt_pk_fp8_f32 v22, v28, v31 op_sel:[0,0,1]
	v_fmamk_f32 v28, v72, 0x3d000000, v8
	v_rcp_f32_e32 v8, v3
	v_mul_f32_e32 v3, 0xbfb8aa3b, v17
	v_fmac_f32_e32 v13, 0x3d000000, v77
	v_fmamk_f32 v36, v68, 0x3d000000, v4
	v_exp_f32_e32 v3, v3
	v_mul_f32_e32 v4, 0xbfb8aa3b, v13
	v_add_f32_e32 v6, 1.0, v6
	v_exp_f32_e32 v4, v4
	v_rcp_f32_e32 v6, v6
	v_rcp_f32_e32 v2, v2
	v_add_f32_e32 v3, 1.0, v3
	v_cvt_f32_ubyte0_e32 v25, v61
	v_rcp_f32_e32 v16, v3
	v_add_f32_e32 v3, 1.0, v4
	v_mov_b32_e32 v7, v212
	v_cvt_f32_ubyte1_e32 v27, v61
	v_rcp_f32_e32 v4, v3
	v_pk_mul_f32 v[6:7], v[24:25], v[6:7]
	v_mov_b32_e32 v11, v212
	s_waitcnt vmcnt(0)
	v_lshlrev_b32_e32 v24, 16, v18
	v_cvt_f32_ubyte0_e32 v33, v62
	v_fmac_f32_e32 v9, 0x3d000000, v73
	v_pk_mul_f32 v[10:11], v[26:27], v[10:11]
	v_mov_b32_e32 v3, v212
	v_fmac_f32_e32 v24, v6, v7
	v_and_b32_e32 v6, 0xffff0000, v18
	v_cvt_f32_ubyte2_e32 v37, v62
	v_fmac_f32_e32 v5, 0x3d000000, v69
	v_mov_b32_e32 v30, v9
	v_pk_mul_f32 v[2:3], v[32:33], v[2:3]
	v_mov_b32_e32 v9, v212
	v_fmac_f32_e32 v6, v10, v11
	v_lshlrev_b32_e32 v11, 16, v20
	v_cvt_f32_ubyte1_e32 v35, v62
	v_cvt_f32_ubyte3_e32 v39, v62
	v_mov_b32_e32 v15, v212
	v_pk_mul_f32 v[8:9], v[36:37], v[8:9]
	v_mov_b32_e32 v38, v5
	v_mov_b32_e32 v5, v212
	v_fmac_f32_e32 v11, v2, v3
	v_lshlrev_b32_e32 v3, 16, v21
	v_pk_mul_f32 v[14:15], v[34:35], v[14:15]
	v_pk_mul_f32 v[4:5], v[38:39], v[4:5]
	v_and_b32_e32 v2, 0xffff0000, v20
	v_fmac_f32_e32 v3, v8, v9
	v_and_b32_e32 v8, 0xffff0000, v21
	v_fmac_f32_e32 v2, v14, v15
	v_fmac_f32_e32 v8, v4, v5
	v_med3_f32 v4, v24, s74, v227
	v_med3_f32 v5, v6, s74, v227
	v_mov_b32_e32 v24, 0
	v_cvt_pk_fp8_f32 v24, v4, v5
	v_med3_f32 v4, v11, s74, v227
	v_med3_f32 v2, v2, s74, v227
	v_mov_b32_e32 v25, 0
	v_cvt_f32_ubyte2_e32 v29, v61
	v_cvt_f32_ubyte3_e32 v31, v61
	v_mov_b32_e32 v13, v212
	v_mov_b32_e32 v17, v212
	v_cvt_pk_fp8_f32 v25, v4, v2
	v_pk_mul_f32 v[12:13], v[28:29], v[12:13]
	v_pk_mul_f32 v[16:17], v[30:31], v[16:17]
	v_lshlrev_b32_e32 v7, 16, v19
	v_and_b32_e32 v10, 0xffff0000, v19
	v_fmac_f32_e32 v7, v12, v13
	v_fmac_f32_e32 v10, v16, v17
	v_med3_f32 v6, v7, s74, v227
	v_med3_f32 v7, v10, s74, v227
	v_med3_f32 v2, v3, s74, v227
	v_med3_f32 v3, v8, s74, v227
	v_cvt_pk_fp8_f32 v24, v6, v7 op_sel:[0,0,1]
	v_cvt_pk_fp8_f32 v25, v2, v3 op_sel:[0,0,1]
	v_add_u32_e32 v2, 0xa0, v60
	v_ashrrev_i32_e32 v3, 31, v2
	v_lshlrev_b64 v[2:3], 11, v[2:3]
	v_lshl_add_u64 v[2:3], s[16:17], 0, v[2:3]
	v_permlane16_swap_b32_e32 v22, v24
	v_permlane16_swap_b32_e32 v23, v25
	v_lshl_add_u64 v[2:3], v[2:3], 0, v[58:59]
	s_mov_b64 s[4:5], -1
	global_store_dwordx4 v[2:3], v[22:25], off
	s_cbranch_vccnz .LBB0_885
	s_andn2_b64 vcc, exec, s[8:9]
	s_cbranch_vccnz .LBB0_884
	s_barrier
	s_branch .LBB0_884

; __device__ __forceinline__ unsigned cvt_pk_bf16(float lo, float hi) { unsigned r; asm volatile("v_cvt_pk_bf16_f32 %0, %1, %2" : "=v"(r) : "v"(lo), "v"(hi)); return r; }
; #define EPI_ALD16(dst_, ptr_) asm volatile("global_load_dwordx4 %0, %1, off" : "=v"(dst_) : "v"(ptr_))
;     __device__ __forceinline__ void operator()(EPI_ARGS) const {
;         const float* gb = gtm + (size_t)(u.pm >> 4) * 6 * D;
;         const float* xt = xin + (size_t)u.pm * 256 * D + u.pn * 256;
; #pragma unroll
;         for (int bj = 0; bj < 2; ++bj) { const int col = u.pn * 256 + bj * 128 + wc * 32 + 8 * fq; f32x4 g0, g1, xv[2][4][2];
;             EPI_ALD16(g0, gb + col); EPI_ALD16(g1, gb + col + 4);
; #pragma unroll
;             for (int ai = 0; ai < 2; ++ai)
; #pragma unroll
;                 for (int m = 0; m < 4; ++m) { const unsigned xo = (unsigned)((ai * 128 + wr * 64 + m * 16 + fr) * D + col - u.pn * 256) * 4u;
;                     asm volatile("global_load_dwordx4 %0, %1, %2" : "=v"(xv[ai][m][0]) : "v"(xo), "s"(xt)); asm volatile("global_load_dwordx4 %0, %1, %2 offset:16" : "=v"(xv[ai][m][1]) : "v"(xo), "s"(xt)); }
;             asm volatile("s_waitcnt vmcnt(0)" : "+v"(g0), "+v"(g1), "+v"(xv[0][0][0]), "+v"(xv[0][0][1]), "+v"(xv[0][1][0]), "+v"(xv[0][1][1]), "+v"(xv[0][2][0]), "+v"(xv[0][2][1]), "+v"(xv[0][3][0]), "+v"(xv[0][3][1]));
;             asm volatile("" : "+v"(xv[1][0][0]), "+v"(xv[1][0][1]), "+v"(xv[1][1][0]), "+v"(xv[1][1][1]), "+v"(xv[1][2][0]), "+v"(xv[1][2][1]), "+v"(xv[1][3][0]), "+v"(xv[1][3][1]));
;             g0 = g0 * asc; g1 = g1 * asc;
; #pragma unroll
;             for (int ai = 0; ai < 2; ++ai)
; #pragma unroll
;                 for (int m = 0; m < 4; ++m) { const int row = u.pm * 256 + ai * 128 + wr * 64 + m * 16 + fr; const f32x4 v0 = xv[ai][m][0] + acc[ai][bj][m][0] * g0, v1 = xv[ai][m][1] + acc[ai][bj][m][1] * g1;
;                     u32x4 w; w.x = cvt_pk_bf16(v0[0], v0[1]); w.y = cvt_pk_bf16(v0[2], v0[3]); w.z = cvt_pk_bf16(v1[0], v1[1]); w.w = cvt_pk_bf16(v1[2], v1[3]);
;                     *(u32x4*)(X1 + (size_t)row * D + col) = w; } }
.LBB0_995:
	s_ashr_i32 s14, s36, 4
	s_mul_i32 s14, s14, 6
	s_ashr_i32 s15, s14, 31
	s_lshl_b64 s[14:15], s[14:15], 13
	s_add_u32 s14, s63, s14
	s_addc_u32 s15, s64, s15
	s_ashr_i32 s37, s36, 31
	s_lshl_b64 s[38:39], s[36:37], 21
	s_add_u32 s25, s6, s38
	s_addc_u32 s27, s7, s39
	s_lshl_b32 s40, s72, 8
	s_ashr_i32 s41, s40, 31
	v_or_b32_e32 v244, s40, v195
	s_lshl_b64 s[38:39], s[40:41], 2
	v_ashrrev_i32_e32 v245, 31, v244
	s_add_u32 s38, s25, s38
	v_lshl_add_u64 v[18:19], v[244:245], 2, s[14:15]
	s_addc_u32 s39, s27, s39
	v_lshl_add_u64 v[2:3], v[18:19], 0, 16
	v_lshlrev_b32_e32 v246, 2, v244
	s_lshl_b32 s14, s72, 10
	s_nop 15
	s_nop 15
	global_load_dwordx4 v[20:23], v[18:19], off
	global_load_dwordx4 v[24:27], v[2:3], off
	v_subrev_u32_e32 v2, s14, v246
	v_add_u32_e32 v3, v2, v216
	global_load_dwordx4 v[30:33], v3, s[38:39]
	global_load_dwordx4 v[42:45], v3, s[38:39] offset:16
	v_add_u32_e32 v3, v2, v217
	global_load_dwordx4 v[46:49], v3, s[38:39]
	global_load_dwordx4 v[50:53], v3, s[38:39] offset:16
	v_add_u32_e32 v3, v2, v218
	global_load_dwordx4 v[54:57], v3, s[38:39]
	global_load_dwordx4 v[58:61], v3, s[38:39] offset:16
	v_add_u32_e32 v3, v2, v219
	global_load_dwordx4 v[62:65], v3, s[38:39]
	global_load_dwordx4 v[212:215], v3, s[38:39] offset:16
	v_add_u32_e32 v3, v2, v220
	global_load_dwordx4 v[228:231], v3, s[38:39]
	global_load_dwordx4 v[232:235], v3, s[38:39] offset:16
	v_add_u32_e32 v3, v2, v221
	global_load_dwordx4 v[236:239], v3, s[38:39]
	global_load_dwordx4 v[240:243], v3, s[38:39] offset:16
	v_add_u32_e32 v3, v2, v222
	v_add_u32_e32 v2, v2, v223
	v_lshl_add_u32 v28, s36, 8, v1
	global_load_dwordx4 v[14:17], v3, s[38:39]
	global_load_dwordx4 v[10:13], v3, s[38:39] offset:16
	global_load_dwordx4 v[6:9], v2, s[38:39]
	global_load_dwordx4 v[2:5], v2, s[38:39] offset:16
	v_ashrrev_i32_e32 v29, 31, v28
	s_waitcnt vmcnt(17)
	v_pk_mul_f32 v[38:39], v[22:23], s[20:21] op_sel_hi:[1,0]
	v_pk_mul_f32 v[40:41], v[20:21], s[20:21] op_sel_hi:[1,0]
	s_waitcnt vmcnt(15)
	v_pk_fma_f32 v[20:21], v[192:193], v[38:39], v[32:33]
	v_pk_fma_f32 v[22:23], v[190:191], v[40:41], v[30:31]
	v_pk_mul_f32 v[36:37], v[24:25], s[20:21] op_sel_hi:[1,0]
	v_cvt_pk_bf16_f32 v22, v22, v23
	v_cvt_pk_bf16_f32 v23, v20, v21
	v_lshlrev_b64 v[20:21], 12, v[28:29]
	s_waitcnt vmcnt(14)
	v_pk_fma_f32 v[24:25], v[186:187], v[36:37], v[42:43]
	v_lshl_add_u64 v[20:21], s[10:11], 0, v[20:21]
	v_lshlrev_b64 v[186:187], 1, v[244:245]
	v_pk_mul_f32 v[34:35], v[26:27], s[20:21] op_sel_hi:[1,0]
	v_lshl_add_u64 v[20:21], v[20:21], 0, v[186:187]
	v_pk_fma_f32 v[26:27], v[188:189], v[34:35], v[44:45]
	v_cvt_pk_bf16_f32 v24, v24, v25
	s_waitcnt vmcnt(12)
	v_pk_fma_f32 v[30:31], v[180:181], v[34:35], v[52:53]
	v_cvt_pk_bf16_f32 v25, v26, v27
	global_store_dwordx4 v[20:21], v[22:25], off
	v_pk_fma_f32 v[26:27], v[184:185], v[38:39], v[48:49]
	v_pk_fma_f32 v[32:33], v[178:179], v[36:37], v[50:51]
	v_or_b32_e32 v22, 16, v28
	v_ashrrev_i32_e32 v23, 31, v22
	v_lshlrev_b64 v[22:23], 12, v[22:23]
	v_pk_fma_f32 v[24:25], v[182:183], v[40:41], v[46:47]
	v_lshl_add_u64 v[22:23], s[10:11], 0, v[22:23]
	v_cvt_pk_bf16_f32 v24, v24, v25
	v_lshl_add_u64 v[22:23], v[22:23], 0, v[186:187]
	v_cvt_pk_bf16_f32 v25, v26, v27
	v_cvt_pk_bf16_f32 v26, v32, v33
	v_cvt_pk_bf16_f32 v27, v30, v31
	global_store_dwordx4 v[22:23], v[24:27], off
	s_waitcnt vmcnt(11)
	v_pk_fma_f32 v[30:31], v[174:175], v[40:41], v[54:55]
	s_waitcnt vmcnt(10)
	v_pk_fma_f32 v[32:33], v[170:171], v[36:37], v[58:59]
	v_or_b32_e32 v24, 32, v28
	v_pk_fma_f32 v[26:27], v[176:177], v[38:39], v[56:57]
	v_ashrrev_i32_e32 v25, 31, v24
	v_cvt_pk_bf16_f32 v30, v30, v31
	v_cvt_pk_bf16_f32 v31, v26, v27
	v_lshlrev_b64 v[24:25], 12, v[24:25]
	v_or_b32_e32 v26, 48, v28
	v_lshl_add_u64 v[24:25], s[10:11], 0, v[24:25]
	v_ashrrev_i32_e32 v27, 31, v26
	v_lshl_add_u64 v[24:25], v[24:25], 0, v[186:187]
	v_lshlrev_b64 v[26:27], 12, v[26:27]
	v_pk_fma_f32 v[42:43], v[172:173], v[34:35], v[60:61]
	v_cvt_pk_bf16_f32 v32, v32, v33
	v_lshl_add_u64 v[26:27], s[10:11], 0, v[26:27]
	v_cvt_pk_bf16_f32 v33, v42, v43
	global_store_dwordx4 v[24:25], v[30:33], off
	v_lshl_add_u64 v[26:27], v[26:27], 0, v[186:187]
	s_waitcnt vmcnt(8)
	v_pk_fma_f32 v[42:43], v[164:165], v[34:35], v[214:215]
	v_pk_fma_f32 v[30:31], v[166:167], v[40:41], v[62:63]
	v_pk_fma_f32 v[32:33], v[168:169], v[38:39], v[64:65]
	v_cvt_pk_bf16_f32 v30, v30, v31
	v_pk_fma_f32 v[44:45], v[162:163], v[36:37], v[212:213]
	v_cvt_pk_bf16_f32 v31, v32, v33
	s_waitcnt vmcnt(6)
	v_pk_fma_f32 v[46:47], v[156:157], v[34:35], v[234:235]
	v_cvt_pk_bf16_f32 v32, v44, v45
	v_cvt_pk_bf16_f32 v33, v42, v43
	global_store_dwordx4 v[26:27], v[30:33], off
	v_pk_fma_f32 v[42:43], v[158:159], v[40:41], v[228:229]
	v_pk_fma_f32 v[44:45], v[154:155], v[36:37], v[232:233]
	v_add_u32_e32 v30, 0x80, v28
	v_pk_fma_f32 v[32:33], v[160:161], v[38:39], v[230:231]
	v_ashrrev_i32_e32 v31, 31, v30
	v_cvt_pk_bf16_f32 v42, v42, v43
	v_cvt_pk_bf16_f32 v43, v32, v33
	v_lshlrev_b64 v[30:31], 12, v[30:31]
	v_add_u32_e32 v32, 0x90, v28
	v_lshl_add_u64 v[30:31], s[10:11], 0, v[30:31]
	v_ashrrev_i32_e32 v33, 31, v32
	v_lshl_add_u64 v[30:31], v[30:31], 0, v[186:187]
	v_lshlrev_b64 v[32:33], 12, v[32:33]
	v_cvt_pk_bf16_f32 v44, v44, v45
	v_cvt_pk_bf16_f32 v45, v46, v47
	global_store_dwordx4 v[30:31], v[42:45], off
	v_lshl_add_u64 v[32:33], s[10:11], 0, v[32:33]
	v_lshl_add_u64 v[32:33], v[32:33], 0, v[186:187]
	s_waitcnt vmcnt(5)
	v_pk_fma_f32 v[42:43], v[150:151], v[40:41], v[236:237]
	v_pk_fma_f32 v[44:45], v[152:153], v[38:39], v[238:239]
	v_cvt_pk_bf16_f32 v42, v42, v43
	s_waitcnt vmcnt(4)
; __device__ __forceinline__ unsigned cvt_pk_bf16(float lo, float hi) { unsigned r; asm volatile("v_cvt_pk_bf16_f32 %0, %1, %2" : "=v"(r) : "v"(lo), "v"(hi)); return r; }
; #define EPI_ALD16(dst_, ptr_) asm volatile("global_load_dwordx4 %0, %1, off" : "=v"(dst_) : "v"(ptr_))
;     __device__ __forceinline__ void operator()(EPI_ARGS) const {
;     ...
;         for (int bj = 0; bj < 2; ++bj) { const int col = u.pn * 256 + bj * 128 + wc * 32 + 8 * fq; f32x4 g0, g1, xv[2][4][2];
;             EPI_ALD16(g0, gb + col); EPI_ALD16(g1, gb + col + 4);
; #pragma unroll
;             for (int ai = 0; ai < 2; ++ai)
; #pragma unroll
;                 for (int m = 0; m < 4; ++m) { const unsigned xo = (unsigned)((ai * 128 + wr * 64 + m * 16 + fr) * D + col - u.pn * 256) * 4u;
;                     asm volatile("global_load_dwordx4 %0, %1, %2" : "=v"(xv[ai][m][0]) : "v"(xo), "s"(xt)); asm volatile("global_load_dwordx4 %0, %1, %2 offset:16" : "=v"(xv[ai][m][1]) : "v"(xo), "s"(xt)); }
;             asm volatile("s_waitcnt vmcnt(0)" : "+v"(g0), "+v"(g1), "+v"(xv[0][0][0]), "+v"(xv[0][0][1]), "+v"(xv[0][1][0]), "+v"(xv[0][1][1]), "+v"(xv[0][2][0]), "+v"(xv[0][2][1]), "+v"(xv[0][3][0]), "+v"(xv[0][3][1]));
;             asm volatile("" : "+v"(xv[1][0][0]), "+v"(xv[1][0][1]), "+v"(xv[1][1][0]), "+v"(xv[1][1][1]), "+v"(xv[1][2][0]), "+v"(xv[1][2][1]), "+v"(xv[1][3][0]), "+v"(xv[1][3][1]));
;             g0 = g0 * asc; g1 = g1 * asc;
; #pragma unroll
;             for (int ai = 0; ai < 2; ++ai)
; #pragma unroll
;                 for (int m = 0; m < 4; ++m) { const int row = u.pm * 256 + ai * 128 + wr * 64 + m * 16 + fr; const f32x4 v0 = xv[ai][m][0] + acc[ai][bj][m][0] * g0, v1 = xv[ai][m][1] + acc[ai][bj][m][1] * g1;
;                     u32x4 w; w.x = cvt_pk_bf16(v0[0], v0[1]); w.y = cvt_pk_bf16(v0[2], v0[3]); w.z = cvt_pk_bf16(v1[0], v1[1]); w.w = cvt_pk_bf16(v1[2], v1[3]);
;                     *(u32x4*)(X1 + (size_t)row * D + col) = w; } }
	v_pk_fma_f32 v[46:47], v[148:149], v[34:35], v[242:243]
	v_pk_fma_f32 v[48:49], v[146:147], v[36:37], v[240:241]
	v_cvt_pk_bf16_f32 v43, v44, v45
	s_waitcnt vmcnt(3)
	v_pk_fma_f32 v[14:15], v[142:143], v[40:41], v[14:15]
	v_cvt_pk_bf16_f32 v44, v48, v49
	v_cvt_pk_bf16_f32 v45, v46, v47
	global_store_dwordx4 v[32:33], v[42:45], off
	s_waitcnt vmcnt(2)
	v_pk_fma_f32 v[10:11], v[138:139], v[36:37], v[10:11]
	v_pk_fma_f32 v[16:17], v[144:145], v[38:39], v[16:17]
	v_add_u32_e32 v42, 0xa0, v28
	v_ashrrev_i32_e32 v43, 31, v42
	v_pk_fma_f32 v[44:45], v[140:141], v[34:35], v[12:13]
	v_cvt_pk_bf16_f32 v12, v14, v15
	v_cvt_pk_bf16_f32 v13, v16, v17
	v_cvt_pk_bf16_f32 v14, v10, v11
	v_lshlrev_b64 v[10:11], 12, v[42:43]
	v_lshl_add_u64 v[10:11], s[10:11], 0, v[10:11]
	v_lshl_add_u64 v[10:11], v[10:11], 0, v[186:187]
	v_cvt_pk_bf16_f32 v15, v44, v45
	global_store_dwordx4 v[10:11], v[12:15], off
	s_waitcnt vmcnt(1)
	v_pk_fma_f32 v[6:7], v[134:135], v[40:41], v[6:7]
	s_waitcnt vmcnt(0)
	v_pk_fma_f32 v[2:3], v[130:131], v[36:37], v[2:3]
	v_add_u32_e32 v12, 0xb0, v28
	v_ashrrev_i32_e32 v13, 31, v12
	v_pk_fma_f32 v[8:9], v[136:137], v[38:39], v[8:9]
	v_pk_fma_f32 v[14:15], v[132:133], v[34:35], v[4:5]
	v_cvt_pk_bf16_f32 v4, v6, v7
	v_cvt_pk_bf16_f32 v5, v8, v9
	v_cvt_pk_bf16_f32 v6, v2, v3
	v_lshlrev_b64 v[2:3], 12, v[12:13]
	v_lshl_add_u64 v[2:3], s[10:11], 0, v[2:3]
	v_lshl_add_u64 v[2:3], v[2:3], 0, v[186:187]
	v_cvt_pk_bf16_f32 v7, v14, v15
	global_store_dwordx4 v[2:3], v[4:7], off
	v_lshl_add_u64 v[8:9], v[18:19], 0, s[22:23]
	s_andn2_b64 vcc, exec, s[4:5]
	v_lshl_add_u64 v[4:5], v[18:19], 0, s[16:17]
	global_load_dwordx4 v[4:7], v[4:5], off
	global_load_dwordx4 v[12:15], v[8:9], off
	v_or_b32_e32 v8, 0x200, v246
	v_subrev_u32_e32 v8, s14, v8
	v_add_u32_e32 v9, v8, v216
	global_load_dwordx4 v[16:19], v9, s[38:39]
	global_load_dwordx4 v[34:37], v9, s[38:39] offset:16
	v_add_u32_e32 v9, v8, v217
	global_load_dwordx4 v[38:41], v9, s[38:39]
	global_load_dwordx4 v[42:45], v9, s[38:39] offset:16
	v_add_u32_e32 v9, v8, v218
	global_load_dwordx4 v[46:49], v9, s[38:39]
	global_load_dwordx4 v[50:53], v9, s[38:39] offset:16
	v_add_u32_e32 v9, v8, v219
	global_load_dwordx4 v[54:57], v9, s[38:39]
	global_load_dwordx4 v[58:61], v9, s[38:39] offset:16
	v_add_u32_e32 v9, v8, v220
	global_load_dwordx4 v[62:65], v9, s[38:39]
	global_load_dwordx4 v[130:133], v9, s[38:39] offset:16
	v_add_u32_e32 v9, v8, v221
	global_load_dwordx4 v[134:137], v9, s[38:39]
	global_load_dwordx4 v[138:141], v9, s[38:39] offset:16
	v_add_u32_e32 v9, v8, v222
	v_add_u32_e32 v8, v8, v223
	global_load_dwordx4 v[142:145], v9, s[38:39]
	global_load_dwordx4 v[146:149], v9, s[38:39] offset:16
	global_load_dwordx4 v[150:153], v8, s[38:39]
	global_load_dwordx4 v[154:157], v8, s[38:39] offset:16
	s_mov_b64 s[4:5], -1
	s_waitcnt vmcnt(17)
	v_pk_mul_f32 v[8:9], v[6:7], s[20:21] op_sel_hi:[1,0]
	v_pk_mul_f32 v[28:29], v[4:5], s[20:21] op_sel_hi:[1,0]
	s_waitcnt vmcnt(16)
	v_pk_mul_f32 v[14:15], v[14:15], s[20:21] op_sel_hi:[1,0]
	v_pk_mul_f32 v[12:13], v[12:13], s[20:21] op_sel_hi:[1,0]
	s_waitcnt vmcnt(15)
	v_pk_fma_f32 v[6:7], v[128:129], v[8:9], v[18:19]
	v_pk_fma_f32 v[4:5], v[126:127], v[28:29], v[16:17]
	s_waitcnt vmcnt(14)
	v_pk_fma_f32 v[16:17], v[124:125], v[14:15], v[36:37]
	v_pk_fma_f32 v[18:19], v[122:123], v[12:13], v[34:35]
	v_cvt_pk_bf16_f32 v4, v4, v5
	v_cvt_pk_bf16_f32 v5, v6, v7
	s_nop 0
	v_cvt_pk_bf16_f32 v6, v18, v19
	v_cvt_pk_bf16_f32 v7, v16, v17
	global_store_dwordx4 v[20:21], v[4:7], off offset:256
	s_waitcnt vmcnt(12)
	v_pk_fma_f32 v[16:17], v[116:117], v[14:15], v[44:45]
	v_pk_fma_f32 v[18:19], v[114:115], v[12:13], v[42:43]
	v_pk_fma_f32 v[6:7], v[120:121], v[8:9], v[40:41]
	v_pk_fma_f32 v[4:5], v[118:119], v[28:29], v[38:39]
	s_nop 0
	v_cvt_pk_bf16_f32 v4, v4, v5
	v_cvt_pk_bf16_f32 v5, v6, v7
	v_cvt_pk_bf16_f32 v6, v18, v19
	v_cvt_pk_bf16_f32 v7, v16, v17
	global_store_dwordx4 v[22:23], v[4:7], off offset:256
	s_waitcnt vmcnt(10)
	v_pk_fma_f32 v[16:17], v[100:101], v[14:15], v[52:53]
	v_pk_fma_f32 v[18:19], v[98:99], v[12:13], v[50:51]
	v_pk_fma_f32 v[6:7], v[112:113], v[8:9], v[48:49]
	v_pk_fma_f32 v[4:5], v[110:111], v[28:29], v[46:47]
	s_nop 0
	v_cvt_pk_bf16_f32 v4, v4, v5
	v_cvt_pk_bf16_f32 v5, v6, v7
	v_cvt_pk_bf16_f32 v6, v18, v19
	v_cvt_pk_bf16_f32 v7, v16, v17
	global_store_dwordx4 v[24:25], v[4:7], off offset:256
	s_waitcnt vmcnt(8)
	v_pk_fma_f32 v[16:17], v[84:85], v[14:15], v[60:61]
	v_pk_fma_f32 v[18:19], v[82:83], v[12:13], v[58:59]
	v_pk_fma_f32 v[6:7], v[88:89], v[8:9], v[56:57]
	v_pk_fma_f32 v[4:5], v[86:87], v[28:29], v[54:55]
	s_nop 0
	v_cvt_pk_bf16_f32 v4, v4, v5
	v_cvt_pk_bf16_f32 v5, v6, v7
	v_cvt_pk_bf16_f32 v6, v18, v19
	v_cvt_pk_bf16_f32 v7, v16, v17
	global_store_dwordx4 v[26:27], v[4:7], off offset:256
	s_waitcnt vmcnt(6)
	v_pk_fma_f32 v[16:17], v[104:105], v[14:15], v[132:133]
	v_pk_fma_f32 v[18:19], v[102:103], v[12:13], v[130:131]
	v_pk_fma_f32 v[6:7], v[108:109], v[8:9], v[64:65]
	v_pk_fma_f32 v[4:5], v[106:107], v[28:29], v[62:63]
	s_nop 0
	v_cvt_pk_bf16_f32 v4, v4, v5
	v_cvt_pk_bf16_f32 v5, v6, v7
	v_cvt_pk_bf16_f32 v6, v18, v19
	v_cvt_pk_bf16_f32 v7, v16, v17
	global_store_dwordx4 v[30:31], v[4:7], off offset:256
	s_waitcnt vmcnt(4)
	v_pk_fma_f32 v[16:17], v[92:93], v[14:15], v[140:141]
	v_pk_fma_f32 v[18:19], v[90:91], v[12:13], v[138:139]
	v_pk_fma_f32 v[6:7], v[96:97], v[8:9], v[136:137]
	v_pk_fma_f32 v[4:5], v[94:95], v[28:29], v[134:135]
	s_nop 0
	v_cvt_pk_bf16_f32 v4, v4, v5
	v_cvt_pk_bf16_f32 v5, v6, v7
	v_cvt_pk_bf16_f32 v6, v18, v19
	v_cvt_pk_bf16_f32 v7, v16, v17
	global_store_dwordx4 v[32:33], v[4:7], off offset:256
	s_waitcnt vmcnt(2)
	v_pk_fma_f32 v[16:17], v[76:77], v[14:15], v[148:149]
	v_pk_fma_f32 v[18:19], v[74:75], v[12:13], v[146:147]
	v_pk_fma_f32 v[6:7], v[80:81], v[8:9], v[144:145]
	v_pk_fma_f32 v[4:5], v[78:79], v[28:29], v[142:143]
	s_nop 0
	v_cvt_pk_bf16_f32 v4, v4, v5
	v_cvt_pk_bf16_f32 v5, v6, v7
	v_cvt_pk_bf16_f32 v6, v18, v19
	v_cvt_pk_bf16_f32 v7, v16, v17
	global_store_dwordx4 v[10:11], v[4:7], off offset:256
	s_waitcnt vmcnt(0)
	v_pk_fma_f32 v[10:11], v[66:67], v[12:13], v[154:155]
	s_nop 0
	v_pk_fma_f32 v[6:7], v[72:73], v[8:9], v[152:153]
	v_pk_fma_f32 v[4:5], v[70:71], v[28:29], v[150:151]
	v_pk_fma_f32 v[8:9], v[68:69], v[14:15], v[156:157]
	v_cvt_pk_bf16_f32 v4, v4, v5
	v_cvt_pk_bf16_f32 v5, v6, v7
	v_cvt_pk_bf16_f32 v6, v10, v11
	s_nop 0
	v_cvt_pk_bf16_f32 v7, v8, v9
	global_store_dwordx4 v[2:3], v[4:7], off offset:256
	s_cbranch_vccnz .LBB0_974
	s_andn2_b64 vcc, exec, s[8:9]
	s_cbranch_vccnz .LBB0_973
	s_barrier
	s_branch .LBB0_973
